# P10 is VALU-bound after the sorted gather: V side takes unmasked bytes (F = sum c(16hi+lo), H = 16 sum c hi; 2 masks instead of 6 ops per pair-dword), dot8 chains start from inline 0
# speedup vs baseline: 1.0232x; 1.0232x over previous
; __device__ __forceinline__ void expert_tokens(const unsigned char* __restrict__ UV, const float* __restrict__ US, const float* __restrict__ VS, ...
;     ...
;         float sy = 0.f;
;         const float sumc = wave_sum(sumc_l) * (0.25f / 4096.f);
; #pragma unroll
;         for (int i = 0; i < 16; ++i) { acc[i] = acc[i] * 4096.f - 7.5f * sumc; sy += acc[i] * acc[i]; }
;         const float ry = rsqrtf(wave_sum(sy) * (1.f / 1024.f) + EPS);
.LBB0_1013:
	v_add_f32_dpp v66, v252, v252 quad_perm:[1,0,3,2] row_mask:0xf bank_mask:0xf bound_ctrl:1
	s_ashr_i32 s21, s20, 31
	s_lshl_b64 s[4:5], s[20:21], 12
	v_add_f32_dpp v66, v66, v66 quad_perm:[2,3,0,1] row_mask:0xf bank_mask:0xf bound_ctrl:1
	v_lshl_add_u64 v[162:163], v[200:201], 0, s[4:5]
	s_waitcnt vmcnt(31)
	v_mov_b64_e32 v[190:191], v[80:81]
	v_add_f32_dpp v66, v66, v66 row_ror:4 row_mask:0xf bank_mask:0xf bound_ctrl:1
	s_waitcnt vmcnt(30)
	v_mov_b64_e32 v[186:187], v[76:77]
	s_waitcnt vmcnt(29)
	v_mov_b64_e32 v[182:183], v[88:89]
	v_add_f32_dpp v66, v66, v66 row_ror:8 row_mask:0xf bank_mask:0xf bound_ctrl:1
	v_mov_b32_e32 v67, v66
	s_nop 1
	v_permlane16_swap_b32_e32 v66, v67
	v_add_f32_e32 v66, v66, v67
	v_mov_b32_e32 v67, v66
	s_nop 1
	v_permlane32_swap_b32_e32 v66, v67
	v_add_f32_e32 v66, v66, v67
	v_mul_f32_e32 v66, 0x38800000, v66
	v_mul_f32_e32 v66, 0x40f00000, v66
	v_pk_add_f32 v[224:225], v[224:225], v[220:221] neg_lo:[0,1] neg_hi:[0,1]
	v_pk_add_f32 v[222:223], v[222:223], v[218:219] neg_lo:[0,1] neg_hi:[0,1]
	v_pk_add_f32 v[216:217], v[216:217], v[212:213] neg_lo:[0,1] neg_hi:[0,1]
	v_pk_add_f32 v[214:215], v[214:215], v[210:211] neg_lo:[0,1] neg_hi:[0,1]
	s_mov_b32 s62, 0x43800000
	v_pk_fma_f32 v[118:119], v[224:225], s[16:17], v[66:67] op_sel_hi:[1,0,0] neg_lo:[0,0,1] neg_hi:[0,0,1]
	v_pk_fma_f32 v[144:145], v[222:223], s[16:17], v[66:67] op_sel_hi:[1,0,0] neg_lo:[0,0,1] neg_hi:[0,0,1]
	v_pk_mul_f32 v[68:69], v[118:119], v[118:119]
	v_pk_mul_f32 v[70:71], v[144:145], v[144:145]
	v_add_f32_e32 v68, v68, v69
	v_pk_fma_f32 v[148:149], v[220:221], s[62:63], v[66:67] op_sel_hi:[1,0,0] neg_lo:[0,0,1] neg_hi:[0,0,1]
	v_add_f32_e32 v68, v70, v68
	v_pk_mul_f32 v[72:73], v[148:149], v[148:149]
	v_add_f32_e32 v68, v71, v68
	v_pk_fma_f32 v[150:151], v[218:219], s[62:63], v[66:67] op_sel_hi:[1,0,0] neg_lo:[0,0,1] neg_hi:[0,0,1]
	v_add_f32_e32 v68, v72, v68
	v_pk_mul_f32 v[114:115], v[150:151], v[150:151]
	v_add_f32_e32 v68, v73, v68
	v_pk_fma_f32 v[152:153], v[216:217], s[16:17], v[66:67] op_sel_hi:[1,0,0] neg_lo:[0,0,1] neg_hi:[0,0,1]
	v_add_f32_e32 v68, v114, v68
	v_pk_mul_f32 v[116:117], v[152:153], v[152:153]
	v_add_f32_e32 v68, v115, v68
	v_pk_fma_f32 v[154:155], v[214:215], s[16:17], v[66:67] op_sel_hi:[1,0,0] neg_lo:[0,0,1] neg_hi:[0,0,1]
	v_add_f32_e32 v68, v116, v68
	v_pk_mul_f32 v[146:147], v[154:155], v[154:155]
	v_add_f32_e32 v68, v117, v68
	v_pk_fma_f32 v[156:157], v[212:213], s[62:63], v[66:67] op_sel_hi:[1,0,0] neg_lo:[0,0,1] neg_hi:[0,0,1]
	v_add_f32_e32 v68, v146, v68
	v_pk_mul_f32 v[158:159], v[156:157], v[156:157]
	v_add_f32_e32 v68, v147, v68
	v_pk_fma_f32 v[160:161], v[210:211], s[62:63], v[66:67] op_sel_hi:[1,0,0] neg_lo:[0,0,1] neg_hi:[0,0,1]
	v_add_f32_e32 v68, v158, v68
	v_pk_mul_f32 v[66:67], v[160:161], v[160:161]
	v_add_f32_e32 v68, v159, v68
	v_add_f32_e32 v66, v66, v68
	v_add_f32_e32 v66, v67, v66
	ds_read_b128 v[114:117], v240 offset:8192
	ds_read2st64_b64 v[70:73], v239 offset0:34 offset1:35
	v_add_f32_dpp v66, v66, v66 quad_perm:[1,0,3,2] row_mask:0xf bank_mask:0xf bound_ctrl:1
	s_waitcnt vmcnt(28)
	v_mov_b64_e32 v[178:179], v[84:85]
	s_waitcnt vmcnt(27)
	v_mov_b64_e32 v[174:175], v[96:97]
	v_add_f32_dpp v66, v66, v66 quad_perm:[2,3,0,1] row_mask:0xf bank_mask:0xf bound_ctrl:1
	s_waitcnt vmcnt(26)
; #define LAS __attribute__((address_space(3)))
; __device__ __forceinline__ void expert_tokens(const unsigned char* __restrict__ UV, const float* __restrict__ US, const float* __restrict__ VS, ...
;     ...
;         float sy = 0.f;
;         const float sumc = wave_sum(sumc_l) * (0.25f / 4096.f);
; #pragma unroll
;         for (int i = 0; i < 16; ++i) { acc[i] = acc[i] * 4096.f - 7.5f * sumc; sy += acc[i] * acc[i]; }
;         const float ry = rsqrtf(wave_sum(sy) * (1.f / 1024.f) + EPS);
;         const float pscale = (t < 2048) ? 1.f + pd : 1.f;
; #pragma unroll
;         for (int j = 0; j < 4; ++j) { const f32x4 y = (f32x4){acc[4 * j], acc[4 * j + 1], acc[4 * j + 2], acc[4 * j + 3]};
;             float* op = out + (size_t)t * 1024 + 256 * j + 4 * lane;
;             const u32x2 xw = *(const LAS u32x2*)(xrow + 512 * j + 8 * lane);
;             { const f32x4 ov_ = pscale * (f32x4){__uint_as_float(xw.x << 16), __uint_as_float(xw.x & 0xffff0000u), __uint_as_float(xw.y << 16), __uint_as_float(xw.y & 0xffff0000u)} + pscale * *(const LAS f32x4*)(pvt + 2048 + 256 * j + 4 * lane) * (y * ry); __builtin_nontemporal_store(ov_, (f32x4*)op); } }
;         ci0 = ni0; ci1 = ni1; cg0 = ng0; cg1 = ng1; csu0 = nsu0; csu1 = nsu1; csv0 = nsv0; csv1 = nsv1;
	v_mov_b64_e32 v[170:171], v[92:93]
	v_mov_b64_e32 v[188:189], v[78:79]
	v_add_f32_dpp v66, v66, v66 row_ror:4 row_mask:0xf bank_mask:0xf bound_ctrl:1
	v_mov_b64_e32 v[184:185], v[74:75]
	v_mov_b64_e32 v[180:181], v[86:87]
	v_add_f32_dpp v66, v66, v66 row_ror:8 row_mask:0xf bank_mask:0xf bound_ctrl:1
	v_mov_b32_e32 v67, v66
	s_nop 1
	v_permlane16_swap_b32_e32 v66, v67
	v_add_f32_e32 v66, v66, v67
	v_mov_b32_e32 v67, v66
	s_nop 1
	v_permlane32_swap_b32_e32 v66, v67
	v_add_f32_e32 v66, v66, v67
	v_fmamk_f32 v66, v66, 0x3a800000, v226
	v_mul_f32_e32 v67, 0x4b800000, v66
	v_cmp_gt_f32_e32 vcc, s9, v66
	v_mov_b64_e32 v[176:177], v[82:83]
	v_mov_b64_e32 v[172:173], v[94:95]
	v_cndmask_b32_e32 v66, v66, v67, vcc
	v_rsq_f32_e32 v66, v66
	v_mov_b64_e32 v[168:169], v[90:91]
	v_mov_b32_e32 v231, v242
	v_mov_b32_e32 v232, v243
	v_mul_f32_e32 v67, 0x45800000, v66
	v_cndmask_b32_e32 v158, v66, v67, vcc
	ds_read2st64_b64 v[66:69], v239 offset0:32 offset1:33
	v_pk_mul_f32 v[166:167], v[144:145], v[158:159] op_sel_hi:[1,0]
	ds_read_b128 v[144:147], v240 offset:9216
	v_pk_mul_f32 v[118:119], v[118:119], v[158:159] op_sel_hi:[1,0]
	s_and_b64 vcc, exec, s[18:19]
	s_waitcnt lgkmcnt(1)
	v_lshlrev_b32_e32 v164, 16, v66
	v_and_b32_e32 v165, 0xffff0000, v66
	v_lshlrev_b32_e32 v66, 16, v67
	v_and_b32_e32 v67, 0xffff0000, v67
	v_pk_fma_f32 v[116:117], v[116:117], v[166:167], v[66:67]
	v_pk_fma_f32 v[114:115], v[114:115], v[118:119], v[164:165]
	global_store_dwordx4 v[162:163], v[114:117], off nt
	v_lshlrev_b32_e32 v66, 16, v68
	v_and_b32_e32 v67, 0xffff0000, v68
	v_lshlrev_b32_e32 v68, 16, v69
	v_and_b32_e32 v69, 0xffff0000, v69
	v_pk_mul_f32 v[114:115], v[148:149], v[158:159] op_sel_hi:[1,0]
	v_pk_mul_f32 v[116:117], v[150:151], v[158:159] op_sel_hi:[1,0]
	s_waitcnt lgkmcnt(0)
	v_pk_fma_f32 v[66:67], v[144:145], v[114:115], v[66:67]
	v_pk_fma_f32 v[68:69], v[146:147], v[116:117], v[68:69]
	global_store_dwordx4 v[162:163], v[66:69], off offset:1024 nt
	ds_read_b128 v[66:69], v240 offset:10240
	ds_read_b128 v[114:117], v240 offset:11264
	v_lshlrev_b32_e32 v118, 16, v70
	v_and_b32_e32 v119, 0xffff0000, v70
	v_lshlrev_b32_e32 v70, 16, v71
	v_and_b32_e32 v71, 0xffff0000, v71
	v_pk_mul_f32 v[144:145], v[152:153], v[158:159] op_sel_hi:[1,0]
	v_pk_mul_f32 v[146:147], v[154:155], v[158:159] op_sel_hi:[1,0]
	s_waitcnt lgkmcnt(1)
	v_pk_fma_f32 v[66:67], v[66:67], v[144:145], v[118:119]
	v_pk_fma_f32 v[68:69], v[68:69], v[146:147], v[70:71]
	global_store_dwordx4 v[162:163], v[66:69], off offset:2048 nt
	v_pk_mul_f32 v[70:71], v[156:157], v[158:159] op_sel_hi:[1,0]
	s_waitcnt vmcnt(28)
	v_mov_b64_e32 v[166:167], v[104:105]
	v_lshlrev_b32_e32 v66, 16, v72
	v_and_b32_e32 v67, 0xffff0000, v72
	v_lshlrev_b32_e32 v68, 16, v73
	v_and_b32_e32 v69, 0xffff0000, v73
	v_pk_mul_f32 v[72:73], v[160:161], v[158:159] op_sel_hi:[1,0]
	s_waitcnt lgkmcnt(0)
	v_pk_fma_f32 v[66:67], v[114:115], v[70:71], v[66:67]
	v_pk_fma_f32 v[68:69], v[116:117], v[72:73], v[68:69]
	s_waitcnt vmcnt(26)
	v_mov_b64_e32 v[158:159], v[112:113]
	global_store_dwordx4 v[162:163], v[66:69], off offset:3072 nt
	v_mov_b64_e32 v[162:163], v[100:101]
	v_mov_b64_e32 v[156:157], v[110:111]
	s_waitcnt vmcnt(26)
	v_mov_b64_e32 v[154:155], v[108:109]
	s_waitcnt vmcnt(25)
	v_mov_b64_e32 v[150:151], v[126:127]
	s_waitcnt vmcnt(24)
	v_mov_b64_e32 v[146:147], v[122:123]
	s_waitcnt vmcnt(23)
	v_mov_b64_e32 v[116:117], v[132:133]
	s_waitcnt vmcnt(22)
	v_mov_b64_e32 v[112:113], v[128:129]
	s_waitcnt vmcnt(21)
	v_mov_b64_e32 v[70:71], v[140:141]
	s_waitcnt vmcnt(20)
	v_mov_b64_e32 v[66:67], v[136:137]
	v_mov_b64_e32 v[164:165], v[102:103]
	v_mov_b64_e32 v[160:161], v[98:99]
	v_mov_b64_e32 v[152:153], v[106:107]
	v_mov_b64_e32 v[148:149], v[124:125]
	v_mov_b64_e32 v[144:145], v[120:121]
	v_mov_b64_e32 v[118:119], v[134:135]
	v_mov_b64_e32 v[114:115], v[130:131]
	v_mov_b64_e32 v[72:73], v[142:143]
	v_mov_b64_e32 v[68:69], v[138:139]
	v_mov_b32_e32 v229, v237
	v_mov_b32_e32 v230, v238
	v_mov_b32_e32 v233, v241
	v_mov_b32_e32 v234, v0
	v_mov_b32_e32 v235, v245
	v_mov_b32_e32 v236, v246
	s_mov_b32 s20, s34
	s_cbranch_vccnz .LBB0_1025

.Lp10_nobar_i:
	v_dot8_i32_i4 v88, v248, v70, 0
	v_dot8_i32_i4 v88, v250, v71, v88
	v_dot8_i32_i4 v74, v248, v188, 0
	v_dot8_i32_i4 v75, v248, v184, 0
	v_dot8_i32_i4 v76, v248, v180, 0
	v_lshlrev_b32_e32 v88, 4, v88
	v_dot8_i32_i4 v88, v247, v70, v88
	v_dot8_i32_i4 v77, v248, v176, 0
	v_dot8_i32_i4 v78, v248, v172, 0
	v_dot8_i32_i4 v79, v248, v168, 0
	v_dot8_i32_i4 v80, v248, v164, 0
	v_dot8_i32_i4 v81, v248, v160, 0
	v_dot8_i32_i4 v82, v248, v156, 0
	v_dot8_i32_i4 v83, v248, v152, 0
	v_dot8_i32_i4 v84, v248, v148, 0
	v_dot8_i32_i4 v85, v248, v144, 0
	v_dot8_i32_i4 v86, v248, v116, 0
	v_dot8_i32_i4 v87, v248, v112, 0
	v_dot8_i32_i4 v70, v248, v66, 0
	v_dot8_i32_i4 v74, v250, v189, v74
	v_dot8_i32_i4 v75, v250, v185, v75
	v_dot8_i32_i4 v76, v250, v181, v76
	v_dot8_i32_i4 v77, v250, v177, v77
	v_dot8_i32_i4 v78, v250, v173, v78
	v_dot8_i32_i4 v79, v250, v169, v79
	v_dot8_i32_i4 v80, v250, v165, v80
	v_dot8_i32_i4 v81, v250, v161, v81
	v_dot8_i32_i4 v82, v250, v157, v82
	v_dot8_i32_i4 v83, v250, v153, v83
	v_dot8_i32_i4 v84, v250, v149, v84
	v_dot8_i32_i4 v85, v250, v145, v85
	v_dot8_i32_i4 v86, v250, v117, v86
	v_dot8_i32_i4 v87, v250, v113, v87
	v_dot8_i32_i4 v70, v250, v67, v70
	v_lshlrev_b32_e32 v74, 4, v74
	v_lshlrev_b32_e32 v75, 4, v75
	v_lshlrev_b32_e32 v76, 4, v76
	v_lshlrev_b32_e32 v77, 4, v77
	v_lshlrev_b32_e32 v78, 4, v78
	v_lshlrev_b32_e32 v79, 4, v79
	v_lshlrev_b32_e32 v80, 4, v80
	v_lshlrev_b32_e32 v81, 4, v81
	v_lshlrev_b32_e32 v82, 4, v82
	v_lshlrev_b32_e32 v83, 4, v83
	v_lshlrev_b32_e32 v84, 4, v84
	v_lshlrev_b32_e32 v85, 4, v85
	v_lshlrev_b32_e32 v86, 4, v86
	v_lshlrev_b32_e32 v87, 4, v87
	v_lshlrev_b32_e32 v70, 4, v70
	v_dot8_i32_i4 v74, v247, v188, v74
	v_dot8_i32_i4 v75, v247, v184, v75
	v_dot8_i32_i4 v76, v247, v180, v76
	v_dot8_i32_i4 v77, v247, v176, v77
	v_dot8_i32_i4 v78, v247, v172, v78
	v_dot8_i32_i4 v79, v247, v168, v79
	v_dot8_i32_i4 v80, v247, v164, v80
	v_dot8_i32_i4 v81, v247, v160, v81
	v_dot8_i32_i4 v82, v247, v156, v82
	v_dot8_i32_i4 v83, v247, v152, v83
	v_dot8_i32_i4 v84, v247, v148, v84
	v_dot8_i32_i4 v85, v247, v144, v85
	v_dot8_i32_i4 v86, v247, v116, v86
	v_dot8_i32_i4 v87, v247, v112, v87
	v_dot8_i32_i4 v70, v247, v66, v70
	v_dot8_i32_i4 v74, v249, v189, v74
	v_dot8_i32_i4 v75, v249, v185, v75
	v_dot8_i32_i4 v76, v249, v181, v76
	v_dot8_i32_i4 v77, v249, v177, v77
	v_dot8_i32_i4 v78, v249, v173, v78
	v_dot8_i32_i4 v79, v249, v169, v79
	v_dot8_i32_i4 v80, v249, v165, v80
	v_dot8_i32_i4 v81, v249, v161, v81
	v_dot8_i32_i4 v82, v249, v157, v82
	v_dot8_i32_i4 v83, v249, v153, v83
	v_dot8_i32_i4 v84, v249, v149, v84
	v_dot8_i32_i4 v85, v249, v145, v85
	v_dot8_i32_i4 v86, v249, v117, v86
	v_dot8_i32_i4 v87, v249, v113, v87
	v_dot8_i32_i4 v88, v249, v71, v88
	v_dot8_i32_i4 v70, v249, v67, v70
	v_permlane32_swap_b32_e32 v74, v82
	v_permlane32_swap_b32_e32 v75, v83
	v_permlane32_swap_b32_e32 v76, v84
	v_permlane32_swap_b32_e32 v77, v85
	v_permlane32_swap_b32_e32 v78, v86
	v_permlane32_swap_b32_e32 v79, v87
	v_permlane32_swap_b32_e32 v80, v88
	v_permlane32_swap_b32_e32 v81, v70
	v_add_u32_e32 v66, v74, v82
	v_add_u32_e32 v67, v75, v83
	v_add_u32_e32 v71, v76, v84
	v_add_u32_e32 v74, v77, v85
	v_add_u32_e32 v75, v78, v86
	v_add_u32_e32 v76, v79, v87
	v_add_u32_e32 v77, v80, v88
	v_add_u32_e32 v70, v81, v70
	v_permlane16_swap_b32_e32 v66, v75
	v_permlane16_swap_b32_e32 v67, v76
	v_permlane16_swap_b32_e32 v71, v77
	v_permlane16_swap_b32_e32 v74, v70
	v_add_u32_e32 v66, v66, v75
	v_add_u32_e32 v67, v67, v76
	v_add_u32_e32 v71, v71, v77
	v_add_u32_e32 v70, v74, v70
	v_cndmask_b32_e64 v74, v71, v66, s[0:1]
	v_cndmask_b32_e64 v66, v66, v71, s[0:1]
	v_cndmask_b32_e64 v71, v70, v67, s[0:1]
	v_cndmask_b32_e64 v67, v67, v70, s[0:1]
	v_add_u32_dpp v66, v66, v74 quad_perm:[2,3,0,1] row_mask:0xf bank_mask:0xf bound_ctrl:1
	s_sub_i32 s4, s21, 32
	v_add_u32_dpp v67, v67, v71 quad_perm:[2,3,0,1] row_mask:0xf bank_mask:0xf bound_ctrl:1
	v_cndmask_b32_e64 v70, v67, v66, s[2:3]
	v_cndmask_b32_e64 v66, v66, v67, s[2:3]
	s_cmp_lt_u32 s25, 4
	s_cselect_b64 vcc, -1, 0
	v_add_u32_dpp v66, v66, v70 quad_perm:[1,0,3,2] row_mask:0xf bank_mask:0xf bound_ctrl:1
	v_cndmask_b32_e32 v70, v234, v233, vcc
	v_cndmask_b32_e32 v71, v230, v229, vcc
	v_add_u32_dpp v66, v66, v66 row_ror:8 row_mask:0xf bank_mask:0xf bound_ctrl:1
	s_cmp_eq_u32 s21, 32
	s_nop 0
	v_add_u32_dpp v67, v66, v66 row_ror:4 row_mask:0xf bank_mask:0xf bound_ctrl:1
	v_and_or_b32 v66, s4, 32, v193
	v_lshlrev_b32_e32 v66, 2, v66
	v_cvt_f32_i32_e32 v74, v67
	ds_bpermute_b32 v75, v66, v70
	v_and_b32_e32 v67, 0xffff0000, v71
	ds_bpermute_b32 v76, v66, v67
	v_add_f32_e32 v71, v251, v74
	v_mul_f32_e32 v71, v244, v71
	s_waitcnt lgkmcnt(1)
	v_mul_f32_e32 v74, v71, v75
	v_fma_f32 v71, |v74|, s28, 1.0
	v_rcp_f32_e32 v75, v71
	v_mul_f32_e32 v79, v74, v74
	v_mul_f32_e32 v79, 0xbf38aa3b, v79
	v_exp_f32_e32 v79, v79
	v_fmamk_f32 v78, v75, 0x3f07dc22, v227
	v_fmaak_f32 v78, v75, v78, 0x3f35f0e3
	v_fmaak_f32 v78, v75, v78, 0xbe11a98e
	v_cndmask_b32_e32 v71, v236, v235, vcc
	v_fmaak_f32 v78, v75, v78, 0x3e027906
	ds_bpermute_b32 v77, v66, v71
	v_mul_f32_e32 v75, v75, v78
	v_mul_f32_e32 v75, v79, v75
	v_mul_f32_e32 v78, v74, v75
	v_fma_f32 v75, -v74, v75, v74
	v_cmp_gt_f32_e32 vcc, 0, v74
	s_nop 1
	v_cndmask_b32_e32 v74, v75, v78, vcc
	s_waitcnt lgkmcnt(1)
	v_mul_f32_e32 v74, v74, v76
	s_cselect_b64 vcc, -1, 0
	s_cmp_gt_u32 s25, 5
	s_waitcnt lgkmcnt(0)
; __device__ __forceinline__ void expert_tokens(const unsigned char* __restrict__ UV, const float* __restrict__ US, const float* __restrict__ VS, ...
;     ...
;         const unsigned nw0 = (unsigned)IDX[(size_t)tn * 128 + lane], nw1 = (unsigned)IDX[(size_t)tn * 128 + 64 + lane];
;         const int ni0 = (int)nw0 & rmask, ni1 = (int)nw1 & rmask;
;         const float ng0 = __uint_as_float(nw0 & 0xFFFF0000u), ng1 = __uint_as_float(nw1 & 0xFFFF0000u);
	v_mul_f32_e32 v74, v74, v77
	s_cselect_b64 s[22:23], -1, 0
	s_cmp_lt_u32 s25, 6
	v_fma_mixlo_f16 v116, v74, s16, 0
	s_cselect_b64 s[4:5], -1, 0
	v_and_b32_e32 v117, 0xffff, v116
	v_cndmask_b32_e64 v74, v242, v232, s[4:5]
	s_add_i32 s24, s21, 1
	s_add_i32 s35, s21, 2
	s_add_i32 s36, s21, 3
	s_add_i32 s37, s21, 4
	s_add_i32 s38, s21, 5
	s_add_i32 s39, s21, 6
	s_add_i32 s40, s21, 7
	s_add_i32 s49, s21, 8
	s_add_i32 s50, s21, 9
	s_add_i32 s51, s21, 10
	s_add_i32 s52, s21, 11
	s_add_i32 s53, s21, 12
	s_add_i32 s54, s21, 13
	s_add_i32 s55, s21, 14
	s_add_i32 s56, s21, 15
	v_cndmask_b32_e32 v136, v74, v231, vcc
	v_readlane_b32 s47, v117, 0
	v_readlane_b32 s48, v117, 1
	s_cmp_lg_u32 s21, 32
	v_readlane_b32 s4, v136, s21
	s_nop 1
	v_lshl_or_b32 v74, s4, 10, v194
	v_readlane_b32 s4, v136, s24
	s_nop 1
	v_lshl_or_b32 v75, s4, 10, v194
	global_load_dwordx4 v[78:81], v74, s[10:11]
	s_nop 0
	global_load_dwordx4 v[74:77], v75, s[10:11]
	v_readlane_b32 s45, v117, 2
	v_readlane_b32 s46, v117, 3
	v_readlane_b32 s4, v136, s35
	s_nop 1
	v_lshl_or_b32 v82, s4, 10, v194
	v_readlane_b32 s4, v136, s36
	s_nop 1
	v_lshl_or_b32 v83, s4, 10, v194
	global_load_dwordx4 v[86:89], v82, s[10:11]
	s_nop 0
	global_load_dwordx4 v[82:85], v83, s[10:11]
	v_readlane_b32 s43, v117, 16
	v_readlane_b32 s44, v117, 17
	v_readlane_b32 s4, v136, s37
	s_nop 1
	v_lshl_or_b32 v90, s4, 10, v194
	v_readlane_b32 s4, v136, s38
	s_nop 1
	v_lshl_or_b32 v91, s4, 10, v194
	global_load_dwordx4 v[94:97], v90, s[10:11]
	s_nop 0
	global_load_dwordx4 v[90:93], v91, s[10:11]
	v_readlane_b32 s41, v117, 18
	v_readlane_b32 s42, v117, 19
	v_readlane_b32 s4, v136, s39
	s_nop 1
	v_lshl_or_b32 v98, s4, 10, v194
	v_readlane_b32 s4, v136, s40
	s_nop 1
	v_lshl_or_b32 v99, s4, 10, v194
	global_load_dwordx4 v[102:105], v98, s[10:11]
	s_nop 0
	global_load_dwordx4 v[98:101], v99, s[10:11]
	v_readlane_b32 s39, v117, 32
	v_readlane_b32 s40, v117, 33
	v_readlane_b32 s4, v136, s49
	s_nop 1
	v_lshl_or_b32 v106, s4, 10, v194
	v_readlane_b32 s4, v136, s50
	s_nop 1
	v_lshl_or_b32 v107, s4, 10, v194
	global_load_dwordx4 v[110:113], v106, s[10:11]
	s_nop 0
	global_load_dwordx4 v[106:109], v107, s[10:11]
	v_readlane_b32 s37, v117, 34
	v_readlane_b32 s38, v117, 35
	v_readlane_b32 s4, v136, s51
	s_nop 1
	v_lshl_or_b32 v120, s4, 10, v194
	v_readlane_b32 s4, v136, s52
	s_nop 1
	v_lshl_or_b32 v121, s4, 10, v194
	global_load_dwordx4 v[124:127], v120, s[10:11]
	s_nop 0
	global_load_dwordx4 v[120:123], v121, s[10:11]
	v_readlane_b32 s35, v117, 48
	v_readlane_b32 s36, v117, 49
	v_readlane_b32 s4, v136, s53
	s_nop 1
	v_lshl_or_b32 v128, s4, 10, v194
	v_readlane_b32 s4, v136, s54
	s_nop 1
	v_lshl_or_b32 v129, s4, 10, v194
	global_load_dwordx4 v[132:135], v128, s[10:11]
	s_nop 0
	global_load_dwordx4 v[128:131], v129, s[10:11]
	v_readlane_b32 s4, v117, 50
	v_readlane_b32 s5, v117, 51
	v_readlane_b32 s24, v136, s55
	s_nop 1
	v_lshl_or_b32 v117, s24, 10, v194
	v_readlane_b32 s24, v136, s56
	s_nop 1
	v_lshl_or_b32 v136, s24, 10, v194
	global_load_dwordx4 v[140:143], v117, s[10:11]
	s_nop 0
	global_load_dwordx4 v[136:139], v136, s[10:11]
	s_cbranch_scc1 .LBB0_1021
	s_waitcnt vmcnt(16)
	s_bfe_i32 s60, s34, 0x10000
	v_alignbit_b32 v237, v237, v237, 16
	v_alignbit_b32 v238, v238, v238, 16
	v_xor_b32_e32 v237, s60, v237
	v_xor_b32_e32 v238, s60, v238
	s_nop 1
	s_mov_b32 s58, 0x99999999
	s_mov_b32 s59, 0x99999999
	v_min_u32_dpp v202, v237, v237 quad_perm:[1,0,3,2] row_mask:0xf bank_mask:0xf
	v_max_u32_dpp v203, v237, v237 quad_perm:[1,0,3,2] row_mask:0xf bank_mask:0xf
	v_min_u32_dpp v204, v238, v238 quad_perm:[1,0,3,2] row_mask:0xf bank_mask:0xf
	v_max_u32_dpp v205, v238, v238 quad_perm:[1,0,3,2] row_mask:0xf bank_mask:0xf
	v_cndmask_b32_e64 v237, v203, v202, s[58:59]
	v_cndmask_b32_e64 v238, v205, v204, s[58:59]
	s_mov_b32 s58, 0xcc33cc33
	s_mov_b32 s59, 0xcc33cc33
	v_min_u32_dpp v202, v237, v237 quad_perm:[2,3,0,1] row_mask:0xf bank_mask:0xf
	v_max_u32_dpp v203, v237, v237 quad_perm:[2,3,0,1] row_mask:0xf bank_mask:0xf
	v_min_u32_dpp v204, v238, v238 quad_perm:[2,3,0,1] row_mask:0xf bank_mask:0xf
	v_max_u32_dpp v205, v238, v238 quad_perm:[2,3,0,1] row_mask:0xf bank_mask:0xf
	v_cndmask_b32_e64 v237, v203, v202, s[58:59]
	v_cndmask_b32_e64 v238, v205, v204, s[58:59]
	s_mov_b32 s58, 0xaa55aa55
	s_mov_b32 s59, 0xaa55aa55
	v_min_u32_dpp v202, v237, v237 quad_perm:[1,0,3,2] row_mask:0xf bank_mask:0xf
	v_max_u32_dpp v203, v237, v237 quad_perm:[1,0,3,2] row_mask:0xf bank_mask:0xf
	v_min_u32_dpp v204, v238, v238 quad_perm:[1,0,3,2] row_mask:0xf bank_mask:0xf
	v_max_u32_dpp v205, v238, v238 quad_perm:[1,0,3,2] row_mask:0xf bank_mask:0xf
	v_cndmask_b32_e64 v237, v203, v202, s[58:59]
	v_cndmask_b32_e64 v238, v205, v204, s[58:59]
	s_mov_b32 s58, 0xf00ff00f
	s_mov_b32 s59, 0xf00ff00f
	v_min_u32_dpp v202, v237, v237 row_ror:8 row_mask:0xf bank_mask:0xf
	v_max_u32_dpp v203, v237, v237 row_ror:8 row_mask:0xf bank_mask:0xf
	v_min_u32_dpp v204, v238, v238 row_ror:8 row_mask:0xf bank_mask:0xf
	v_max_u32_dpp v205, v238, v238 row_ror:8 row_mask:0xf bank_mask:0xf
	v_cndmask_b32_e64 v237, v203, v202, s[58:59]
	v_cndmask_b32_e64 v238, v205, v204, s[58:59]
	s_mov_b32 s58, 0xc3c3c3c3
	s_mov_b32 s59, 0xc3c3c3c3
	v_min_u32_dpp v202, v237, v237 quad_perm:[2,3,0,1] row_mask:0xf bank_mask:0xf
	v_max_u32_dpp v203, v237, v237 quad_perm:[2,3,0,1] row_mask:0xf bank_mask:0xf
	v_min_u32_dpp v204, v238, v238 quad_perm:[2,3,0,1] row_mask:0xf bank_mask:0xf
	v_max_u32_dpp v205, v238, v238 quad_perm:[2,3,0,1] row_mask:0xf bank_mask:0xf
	v_cndmask_b32_e64 v237, v203, v202, s[58:59]
	v_cndmask_b32_e64 v238, v205, v204, s[58:59]
	s_mov_b32 s58, 0xa5a5a5a5
	s_mov_b32 s59, 0xa5a5a5a5
; __device__ __forceinline__ void expert_tokens(const unsigned char* __restrict__ UV, const float* __restrict__ US, const float* __restrict__ VS, ...
;     ...
;         const unsigned nw0 = (unsigned)IDX[(size_t)tn * 128 + lane], nw1 = (unsigned)IDX[(size_t)tn * 128 + 64 + lane];
;         const int ni0 = (int)nw0 & rmask, ni1 = (int)nw1 & rmask;
;         const float ng0 = __uint_as_float(nw0 & 0xFFFF0000u), ng1 = __uint_as_float(nw1 & 0xFFFF0000u);
	v_min_u32_dpp v202, v237, v237 quad_perm:[1,0,3,2] row_mask:0xf bank_mask:0xf
	v_max_u32_dpp v203, v237, v237 quad_perm:[1,0,3,2] row_mask:0xf bank_mask:0xf
	v_min_u32_dpp v204, v238, v238 quad_perm:[1,0,3,2] row_mask:0xf bank_mask:0xf
	v_max_u32_dpp v205, v238, v238 quad_perm:[1,0,3,2] row_mask:0xf bank_mask:0xf
	v_cndmask_b32_e64 v237, v203, v202, s[58:59]
	v_cndmask_b32_e64 v238, v205, v204, s[58:59]
	s_mov_b32 s58, 0xf0f00f0f
	s_mov_b32 s59, 0xf0f00f0f
	v_mov_b32_dpp v202, v237 row_half_mirror row_mask:0xf bank_mask:0xf
	v_mov_b32_dpp v204, v238 row_half_mirror row_mask:0xf bank_mask:0xf
	s_nop 0
	v_max_u32_dpp v203, v202, v237 quad_perm:[3,2,1,0] row_mask:0xf bank_mask:0xf
	v_max_u32_dpp v205, v204, v238 quad_perm:[3,2,1,0] row_mask:0xf bank_mask:0xf
	v_min_u32_dpp v202, v202, v237 quad_perm:[3,2,1,0] row_mask:0xf bank_mask:0xf
	v_min_u32_dpp v204, v204, v238 quad_perm:[3,2,1,0] row_mask:0xf bank_mask:0xf
	v_cndmask_b32_e64 v237, v203, v202, s[58:59]
	v_cndmask_b32_e64 v238, v205, v204, s[58:59]
	s_mov_b32 s58, 0xff0000ff
	s_mov_b32 s59, 0xff0000ff
	v_min_u32_dpp v202, v237, v237 row_ror:8 row_mask:0xf bank_mask:0xf
	v_max_u32_dpp v203, v237, v237 row_ror:8 row_mask:0xf bank_mask:0xf
	v_min_u32_dpp v204, v238, v238 row_ror:8 row_mask:0xf bank_mask:0xf
	v_max_u32_dpp v205, v238, v238 row_ror:8 row_mask:0xf bank_mask:0xf
	v_cndmask_b32_e64 v237, v203, v202, s[58:59]
	v_cndmask_b32_e64 v238, v205, v204, s[58:59]
	s_mov_b32 s58, 0xcccc3333
	s_mov_b32 s59, 0xcccc3333
	v_min_u32_dpp v202, v237, v237 quad_perm:[2,3,0,1] row_mask:0xf bank_mask:0xf
	v_max_u32_dpp v203, v237, v237 quad_perm:[2,3,0,1] row_mask:0xf bank_mask:0xf
	v_min_u32_dpp v204, v238, v238 quad_perm:[2,3,0,1] row_mask:0xf bank_mask:0xf
	v_max_u32_dpp v205, v238, v238 quad_perm:[2,3,0,1] row_mask:0xf bank_mask:0xf
	v_cndmask_b32_e64 v237, v203, v202, s[58:59]
	v_cndmask_b32_e64 v238, v205, v204, s[58:59]
	s_mov_b32 s58, 0xaaaa5555
	s_mov_b32 s59, 0xaaaa5555
	v_min_u32_dpp v202, v237, v237 quad_perm:[1,0,3,2] row_mask:0xf bank_mask:0xf
	v_max_u32_dpp v203, v237, v237 quad_perm:[1,0,3,2] row_mask:0xf bank_mask:0xf
	v_min_u32_dpp v204, v238, v238 quad_perm:[1,0,3,2] row_mask:0xf bank_mask:0xf
	v_max_u32_dpp v205, v238, v238 quad_perm:[1,0,3,2] row_mask:0xf bank_mask:0xf
	v_cndmask_b32_e64 v237, v203, v202, s[58:59]
	v_cndmask_b32_e64 v238, v205, v204, s[58:59]
	s_nop 1
	v_permlane16_swap_b32_e32 v237, v238
	s_mov_b32 s58, -1
	s_mov_b32 s59, 0
	v_min_u32_e32 v202, v237, v238
	v_max_u32_e32 v203, v237, v238
	v_cndmask_b32_e64 v237, v203, v202, s[58:59]
	v_cndmask_b32_e64 v238, v202, v203, s[58:59]
	s_mov_b32 s58, 0xf0f0f0f
	s_mov_b32 s59, 0xf0f0f0f0
	v_mov_b32_dpp v202, v237 row_half_mirror row_mask:0xf bank_mask:0xf
	v_mov_b32_dpp v204, v238 row_half_mirror row_mask:0xf bank_mask:0xf
	s_nop 0
	v_max_u32_dpp v203, v202, v237 quad_perm:[3,2,1,0] row_mask:0xf bank_mask:0xf
	v_max_u32_dpp v205, v204, v238 quad_perm:[3,2,1,0] row_mask:0xf bank_mask:0xf
	v_min_u32_dpp v202, v202, v237 quad_perm:[3,2,1,0] row_mask:0xf bank_mask:0xf
	v_min_u32_dpp v204, v204, v238 quad_perm:[3,2,1,0] row_mask:0xf bank_mask:0xf
	v_cndmask_b32_e64 v237, v203, v202, s[58:59]
	v_cndmask_b32_e64 v238, v205, v204, s[58:59]
	s_mov_b32 s58, 0xff00ff
	s_mov_b32 s59, 0xff00ff00
	v_min_u32_dpp v202, v237, v237 row_ror:8 row_mask:0xf bank_mask:0xf
	v_max_u32_dpp v203, v237, v237 row_ror:8 row_mask:0xf bank_mask:0xf
	v_min_u32_dpp v204, v238, v238 row_ror:8 row_mask:0xf bank_mask:0xf
	v_max_u32_dpp v205, v238, v238 row_ror:8 row_mask:0xf bank_mask:0xf
	v_cndmask_b32_e64 v237, v203, v202, s[58:59]
	v_cndmask_b32_e64 v238, v205, v204, s[58:59]
	s_mov_b32 s58, 0x33333333
	s_mov_b32 s59, 0xcccccccc
	v_min_u32_dpp v202, v237, v237 quad_perm:[2,3,0,1] row_mask:0xf bank_mask:0xf
	v_max_u32_dpp v203, v237, v237 quad_perm:[2,3,0,1] row_mask:0xf bank_mask:0xf
	v_min_u32_dpp v204, v238, v238 quad_perm:[2,3,0,1] row_mask:0xf bank_mask:0xf
	v_max_u32_dpp v205, v238, v238 quad_perm:[2,3,0,1] row_mask:0xf bank_mask:0xf
	v_cndmask_b32_e64 v237, v203, v202, s[58:59]
	v_cndmask_b32_e64 v238, v205, v204, s[58:59]
	s_mov_b32 s58, 0x55555555
	s_mov_b32 s59, 0xaaaaaaaa
	v_min_u32_dpp v202, v237, v237 quad_perm:[1,0,3,2] row_mask:0xf bank_mask:0xf
	v_max_u32_dpp v203, v237, v237 quad_perm:[1,0,3,2] row_mask:0xf bank_mask:0xf
	v_min_u32_dpp v204, v238, v238 quad_perm:[1,0,3,2] row_mask:0xf bank_mask:0xf
	v_max_u32_dpp v205, v238, v238 quad_perm:[1,0,3,2] row_mask:0xf bank_mask:0xf
	v_cndmask_b32_e64 v237, v203, v202, s[58:59]
	v_cndmask_b32_e64 v238, v205, v204, s[58:59]
	s_nop 1
	v_permlane32_swap_b32_e32 v237, v238
	s_mov_b32 s58, 0xffff
	s_mov_b32 s59, 0xffff
	v_min_u32_e32 v202, v237, v238
	v_max_u32_e32 v203, v237, v238
	v_cndmask_b32_e64 v237, v203, v202, s[58:59]
	v_cndmask_b32_e64 v238, v202, v203, s[58:59]
	s_nop 1
	v_permlane32_swap_b32_e32 v237, v238
	s_mov_b32 s58, 0xffff
	s_mov_b32 s59, 0xffff
	v_min_u32_e32 v202, v237, v238
	v_max_u32_e32 v203, v237, v238
	v_cndmask_b32_e64 v237, v203, v202, s[58:59]
	v_cndmask_b32_e64 v238, v202, v203, s[58:59]
	s_mov_b32 s58, 0xf0f00f0f
	s_mov_b32 s59, 0xf0f00f0f
	v_mov_b32_dpp v202, v237 row_half_mirror row_mask:0xf bank_mask:0xf
	v_mov_b32_dpp v204, v238 row_half_mirror row_mask:0xf bank_mask:0xf
	s_nop 0
	v_max_u32_dpp v203, v202, v237 quad_perm:[3,2,1,0] row_mask:0xf bank_mask:0xf
	v_max_u32_dpp v205, v204, v238 quad_perm:[3,2,1,0] row_mask:0xf bank_mask:0xf
	v_min_u32_dpp v202, v202, v237 quad_perm:[3,2,1,0] row_mask:0xf bank_mask:0xf
	v_min_u32_dpp v204, v204, v238 quad_perm:[3,2,1,0] row_mask:0xf bank_mask:0xf
	v_cndmask_b32_e64 v237, v203, v202, s[58:59]
	v_cndmask_b32_e64 v238, v205, v204, s[58:59]
; __device__ __forceinline__ void expert_tokens(const unsigned char* __restrict__ UV, const float* __restrict__ US, const float* __restrict__ VS, ...
;     ...
;             if (bi == 0) { nsu0 = US[ni0]; nsu1 = US[ni1]; nsv0 = VS[ni0]; nsv1 = VS[ni1]; }
	s_mov_b32 s58, 0xff0000ff
	s_mov_b32 s59, 0xff0000ff
	v_min_u32_dpp v202, v237, v237 row_ror:8 row_mask:0xf bank_mask:0xf
	v_max_u32_dpp v203, v237, v237 row_ror:8 row_mask:0xf bank_mask:0xf
	v_min_u32_dpp v204, v238, v238 row_ror:8 row_mask:0xf bank_mask:0xf
	v_max_u32_dpp v205, v238, v238 row_ror:8 row_mask:0xf bank_mask:0xf
	v_cndmask_b32_e64 v237, v203, v202, s[58:59]
	v_cndmask_b32_e64 v238, v205, v204, s[58:59]
	s_mov_b32 s58, 0xcccc3333
	s_mov_b32 s59, 0xcccc3333
	v_min_u32_dpp v202, v237, v237 quad_perm:[2,3,0,1] row_mask:0xf bank_mask:0xf
	v_max_u32_dpp v203, v237, v237 quad_perm:[2,3,0,1] row_mask:0xf bank_mask:0xf
	v_min_u32_dpp v204, v238, v238 quad_perm:[2,3,0,1] row_mask:0xf bank_mask:0xf
	v_max_u32_dpp v205, v238, v238 quad_perm:[2,3,0,1] row_mask:0xf bank_mask:0xf
	v_cndmask_b32_e64 v237, v203, v202, s[58:59]
	v_cndmask_b32_e64 v238, v205, v204, s[58:59]
	s_mov_b32 s58, 0xaaaa5555
	s_mov_b32 s59, 0xaaaa5555
	v_min_u32_dpp v202, v237, v237 quad_perm:[1,0,3,2] row_mask:0xf bank_mask:0xf
	v_max_u32_dpp v203, v237, v237 quad_perm:[1,0,3,2] row_mask:0xf bank_mask:0xf
	v_min_u32_dpp v204, v238, v238 quad_perm:[1,0,3,2] row_mask:0xf bank_mask:0xf
	v_max_u32_dpp v205, v238, v238 quad_perm:[1,0,3,2] row_mask:0xf bank_mask:0xf
	v_cndmask_b32_e64 v237, v203, v202, s[58:59]
	v_cndmask_b32_e64 v238, v205, v204, s[58:59]
	s_nop 1
	v_permlane16_swap_b32_e32 v237, v238
	v_min_u32_e32 v202, v237, v238
	v_max_u32_e32 v238, v237, v238
	v_mov_b32_e32 v237, v202
	s_nop 1
	v_permlane32_swap_b32_e32 v237, v238
	v_min_u32_e32 v202, v237, v238
	v_max_u32_e32 v238, v237, v238
	v_mov_b32_e32 v237, v202
	s_nop 1
	v_permlane16_swap_b32_e32 v237, v238
	v_min_u32_e32 v202, v237, v238
	v_max_u32_e32 v238, v237, v238
	v_mov_b32_e32 v237, v202
	s_mov_b32 s58, 0xf0f0f0f
	s_mov_b32 s59, 0xf0f0f0f
	v_mov_b32_dpp v202, v237 row_half_mirror row_mask:0xf bank_mask:0xf
	v_mov_b32_dpp v204, v238 row_half_mirror row_mask:0xf bank_mask:0xf
	s_nop 0
	v_max_u32_dpp v203, v202, v237 quad_perm:[3,2,1,0] row_mask:0xf bank_mask:0xf
	v_max_u32_dpp v205, v204, v238 quad_perm:[3,2,1,0] row_mask:0xf bank_mask:0xf
	v_min_u32_dpp v202, v202, v237 quad_perm:[3,2,1,0] row_mask:0xf bank_mask:0xf
	v_min_u32_dpp v204, v204, v238 quad_perm:[3,2,1,0] row_mask:0xf bank_mask:0xf
	v_cndmask_b32_e64 v237, v203, v202, s[58:59]
	v_cndmask_b32_e64 v238, v205, v204, s[58:59]
	s_mov_b32 s58, 0xff00ff
	s_mov_b32 s59, 0xff00ff
	v_min_u32_dpp v202, v237, v237 row_ror:8 row_mask:0xf bank_mask:0xf
	v_max_u32_dpp v203, v237, v237 row_ror:8 row_mask:0xf bank_mask:0xf
	v_min_u32_dpp v204, v238, v238 row_ror:8 row_mask:0xf bank_mask:0xf
	v_max_u32_dpp v205, v238, v238 row_ror:8 row_mask:0xf bank_mask:0xf
	v_cndmask_b32_e64 v237, v203, v202, s[58:59]
	v_cndmask_b32_e64 v238, v205, v204, s[58:59]
	s_mov_b32 s58, 0x33333333
	s_mov_b32 s59, 0x33333333
	v_min_u32_dpp v202, v237, v237 quad_perm:[2,3,0,1] row_mask:0xf bank_mask:0xf
	v_max_u32_dpp v203, v237, v237 quad_perm:[2,3,0,1] row_mask:0xf bank_mask:0xf
	v_min_u32_dpp v204, v238, v238 quad_perm:[2,3,0,1] row_mask:0xf bank_mask:0xf
	v_max_u32_dpp v205, v238, v238 quad_perm:[2,3,0,1] row_mask:0xf bank_mask:0xf
	v_cndmask_b32_e64 v237, v203, v202, s[58:59]
	v_cndmask_b32_e64 v238, v205, v204, s[58:59]
	s_mov_b32 s58, 0x55555555
	s_mov_b32 s59, 0x55555555
	v_min_u32_dpp v202, v237, v237 quad_perm:[1,0,3,2] row_mask:0xf bank_mask:0xf
	v_max_u32_dpp v203, v237, v237 quad_perm:[1,0,3,2] row_mask:0xf bank_mask:0xf
	v_min_u32_dpp v204, v238, v238 quad_perm:[1,0,3,2] row_mask:0xf bank_mask:0xf
	v_max_u32_dpp v205, v238, v238 quad_perm:[1,0,3,2] row_mask:0xf bank_mask:0xf
	v_cndmask_b32_e64 v237, v203, v202, s[58:59]
	v_cndmask_b32_e64 v238, v205, v204, s[58:59]
	s_nop 1
	v_permlane16_swap_b32_e32 v237, v238
	s_nop 1
	v_permlane32_swap_b32_e32 v237, v238
	v_xor_b32_e32 v237, s60, v237
	v_xor_b32_e32 v238, s60, v238
	v_alignbit_b32 v237, v237, v237, 16
	v_alignbit_b32 v238, v238, v238, 16
	v_and_b32_e32 v242, 0x3fff, v237
	v_and_b32_e32 v243, 0x3fff, v238
	v_lshlrev_b32_e32 v208, 2, v242
	v_lshlrev_b32_e32 v206, 2, v243
	global_load_dword v241, v208, s[12:13]
	global_load_dword v0, v206, s[12:13]
	global_load_dword v245, v208, s[14:15]
	global_load_dword v246, v206, s[14:15]
.LBB0_1021:
	s_lshl_b32 s48, s48, 16
	v_and_b32_e32 v144, 0xf0f0f0f0, v190
	v_and_b32_e32 v148, 0xf0f0f0f0, v186
	s_or_b32 s47, s48, s47
	v_perm_b32 v149, v186, v190, s29
	v_dot2c_f32_f16_e32 v224, s47, v149
	v_perm_b32 v149, v148, v144, s29
	v_dot2c_f32_f16_e32 v220, s47, v149
	v_perm_b32 v149, v186, v190, s30
	v_dot2c_f32_f16_e32 v225, s47, v149
	v_perm_b32 v149, v148, v144, s30
	v_dot2c_f32_f16_e32 v221, s47, v149
	v_perm_b32 v149, v186, v190, s31
	v_perm_b32 v117, v186, v190, s33
	v_dot2c_f32_f16_e32 v223, s47, v117
	v_perm_b32 v117, v148, v144, s33
	v_dot2c_f32_f16_e32 v222, s47, v149
	v_perm_b32 v149, v148, v144, s31
	v_dot2c_f32_f16_e32 v219, s47, v117
	v_and_b32_e32 v144, 0xf0f0f0f0, v191
	v_and_b32_e32 v148, 0xf0f0f0f0, v187
	v_dot2c_f32_f16_e32 v218, s47, v149
	v_perm_b32 v149, v187, v191, s29
	v_dot2c_f32_f16_e32 v216, s47, v149
	v_perm_b32 v149, v148, v144, s29
	v_dot2c_f32_f16_e32 v212, s47, v149
	v_perm_b32 v149, v187, v191, s30
	v_dot2c_f32_f16_e32 v217, s47, v149
	v_perm_b32 v149, v148, v144, s30
	v_dot2c_f32_f16_e32 v213, s47, v149
	v_perm_b32 v149, v187, v191, s31
	v_perm_b32 v117, v187, v191, s33
	v_dot2c_f32_f16_e32 v215, s47, v117
	v_perm_b32 v117, v148, v144, s33
	v_dot2c_f32_f16_e32 v214, s47, v149
	v_perm_b32 v149, v148, v144, s31
	v_dot2c_f32_f16_e32 v211, s47, v117
	s_lshl_b32 s46, s46, 16
	v_and_b32_e32 v144, 0xf0f0f0f0, v182
	v_and_b32_e32 v148, 0xf0f0f0f0, v178
	v_dot2c_f32_f16_e32 v210, s47, v149
	s_or_b32 s45, s46, s45
	v_perm_b32 v149, v178, v182, s29
	v_dot2c_f32_f16_e32 v224, s45, v149
	v_perm_b32 v149, v148, v144, s29
	v_dot2c_f32_f16_e32 v220, s45, v149
	v_perm_b32 v149, v178, v182, s30
	v_dot2c_f32_f16_e32 v225, s45, v149
	v_perm_b32 v149, v148, v144, s30
	v_dot2c_f32_f16_e32 v221, s45, v149
	v_perm_b32 v149, v178, v182, s31
	v_perm_b32 v117, v178, v182, s33
	v_dot2c_f32_f16_e32 v223, s45, v117
	v_perm_b32 v117, v148, v144, s33
	v_dot2c_f32_f16_e32 v222, s45, v149
	v_perm_b32 v149, v148, v144, s31
	v_dot2c_f32_f16_e32 v219, s45, v117
	v_and_b32_e32 v144, 0xf0f0f0f0, v183
	v_and_b32_e32 v148, 0xf0f0f0f0, v179
	v_dot2c_f32_f16_e32 v218, s45, v149
	v_perm_b32 v149, v179, v183, s29
	v_dot2c_f32_f16_e32 v216, s45, v149
	v_perm_b32 v149, v148, v144, s29
	v_dot2c_f32_f16_e32 v212, s45, v149
	v_perm_b32 v149, v179, v183, s30
	v_dot2c_f32_f16_e32 v217, s45, v149
	v_perm_b32 v149, v148, v144, s30
	v_dot2c_f32_f16_e32 v213, s45, v149
	v_perm_b32 v149, v179, v183, s31
	v_perm_b32 v117, v179, v183, s33
	v_dot2c_f32_f16_e32 v215, s45, v117
	v_perm_b32 v117, v148, v144, s33
	v_dot2c_f32_f16_e32 v214, s45, v149
	v_perm_b32 v149, v148, v144, s31
	v_dot2c_f32_f16_e32 v211, s45, v117
	s_lshl_b32 s44, s44, 16
	v_and_b32_e32 v144, 0xf0f0f0f0, v174
	v_and_b32_e32 v148, 0xf0f0f0f0, v170
	v_dot2c_f32_f16_e32 v210, s45, v149
	s_or_b32 s43, s44, s43
	v_perm_b32 v149, v170, v174, s29
	v_dot2c_f32_f16_e32 v224, s43, v149
	v_perm_b32 v149, v148, v144, s29
	v_dot2c_f32_f16_e32 v220, s43, v149
	v_perm_b32 v149, v170, v174, s30
	v_dot2c_f32_f16_e32 v225, s43, v149
	v_perm_b32 v149, v148, v144, s30
	v_dot2c_f32_f16_e32 v221, s43, v149
	v_perm_b32 v149, v170, v174, s31
	v_perm_b32 v117, v170, v174, s33
	v_dot2c_f32_f16_e32 v223, s43, v117
	v_perm_b32 v117, v148, v144, s33
	v_dot2c_f32_f16_e32 v222, s43, v149
	v_perm_b32 v149, v148, v144, s31
	v_dot2c_f32_f16_e32 v219, s43, v117
	v_and_b32_e32 v144, 0xf0f0f0f0, v175
	v_and_b32_e32 v148, 0xf0f0f0f0, v171
	v_dot2c_f32_f16_e32 v218, s43, v149
	v_perm_b32 v149, v171, v175, s29
	v_dot2c_f32_f16_e32 v216, s43, v149
	v_perm_b32 v149, v148, v144, s29
	v_dot2c_f32_f16_e32 v212, s43, v149
	v_perm_b32 v149, v171, v175, s30
	v_dot2c_f32_f16_e32 v217, s43, v149
	v_perm_b32 v149, v148, v144, s30
	v_dot2c_f32_f16_e32 v213, s43, v149
	v_perm_b32 v149, v171, v175, s31
	v_perm_b32 v117, v171, v175, s33
	v_dot2c_f32_f16_e32 v215, s43, v117
	v_perm_b32 v117, v148, v144, s33
	v_dot2c_f32_f16_e32 v214, s43, v149
	v_perm_b32 v149, v148, v144, s31
	v_dot2c_f32_f16_e32 v211, s43, v117
	s_lshl_b32 s42, s42, 16
	v_and_b32_e32 v144, 0xf0f0f0f0, v166
	v_and_b32_e32 v148, 0xf0f0f0f0, v162
	v_dot2c_f32_f16_e32 v210, s43, v149
	s_or_b32 s41, s42, s41
	v_perm_b32 v149, v162, v166, s29
	v_dot2c_f32_f16_e32 v224, s41, v149
	v_perm_b32 v149, v148, v144, s29
	v_dot2c_f32_f16_e32 v220, s41, v149
	v_perm_b32 v149, v162, v166, s30
	v_dot2c_f32_f16_e32 v225, s41, v149
	v_perm_b32 v149, v148, v144, s30
	v_dot2c_f32_f16_e32 v221, s41, v149
	v_perm_b32 v149, v162, v166, s31
	v_perm_b32 v117, v162, v166, s33
	v_dot2c_f32_f16_e32 v223, s41, v117
	v_perm_b32 v117, v148, v144, s33
	v_dot2c_f32_f16_e32 v222, s41, v149
	v_perm_b32 v149, v148, v144, s31
	v_dot2c_f32_f16_e32 v219, s41, v117
	v_and_b32_e32 v144, 0xf0f0f0f0, v167
	v_and_b32_e32 v148, 0xf0f0f0f0, v163
	v_dot2c_f32_f16_e32 v218, s41, v149
	v_perm_b32 v149, v163, v167, s29
	v_dot2c_f32_f16_e32 v216, s41, v149
	v_perm_b32 v149, v148, v144, s29
	v_dot2c_f32_f16_e32 v212, s41, v149
	v_perm_b32 v149, v163, v167, s30
	v_dot2c_f32_f16_e32 v217, s41, v149
	v_perm_b32 v149, v148, v144, s30
	v_dot2c_f32_f16_e32 v213, s41, v149
	v_perm_b32 v149, v163, v167, s31
	v_perm_b32 v117, v163, v167, s33
	v_dot2c_f32_f16_e32 v215, s41, v117
	v_perm_b32 v117, v148, v144, s33
	v_dot2c_f32_f16_e32 v214, s41, v149
	v_perm_b32 v149, v148, v144, s31
	v_dot2c_f32_f16_e32 v211, s41, v117
	s_lshl_b32 s40, s40, 16
	v_and_b32_e32 v144, 0xf0f0f0f0, v158
	v_and_b32_e32 v148, 0xf0f0f0f0, v154
	v_dot2c_f32_f16_e32 v210, s41, v149
	s_or_b32 s39, s40, s39
	v_perm_b32 v149, v154, v158, s29
	v_dot2c_f32_f16_e32 v224, s39, v149
	v_perm_b32 v149, v148, v144, s29
	v_dot2c_f32_f16_e32 v220, s39, v149
	v_perm_b32 v149, v154, v158, s30
	v_dot2c_f32_f16_e32 v225, s39, v149
	v_perm_b32 v149, v148, v144, s30
	v_dot2c_f32_f16_e32 v221, s39, v149
	v_perm_b32 v149, v154, v158, s31
	v_perm_b32 v117, v154, v158, s33
	v_dot2c_f32_f16_e32 v223, s39, v117
	v_perm_b32 v117, v148, v144, s33
	v_dot2c_f32_f16_e32 v222, s39, v149
	v_perm_b32 v149, v148, v144, s31
	v_dot2c_f32_f16_e32 v219, s39, v117
	v_and_b32_e32 v144, 0xf0f0f0f0, v159
	v_and_b32_e32 v148, 0xf0f0f0f0, v155
	v_dot2c_f32_f16_e32 v218, s39, v149
	v_perm_b32 v149, v155, v159, s29
	v_dot2c_f32_f16_e32 v216, s39, v149
	v_perm_b32 v149, v148, v144, s29
	v_dot2c_f32_f16_e32 v212, s39, v149
	v_perm_b32 v149, v155, v159, s30
	v_dot2c_f32_f16_e32 v217, s39, v149
	v_perm_b32 v149, v148, v144, s30
	v_dot2c_f32_f16_e32 v213, s39, v149
	v_perm_b32 v149, v155, v159, s31
	v_perm_b32 v117, v155, v159, s33
	v_dot2c_f32_f16_e32 v215, s39, v117
	v_perm_b32 v117, v148, v144, s33
	v_dot2c_f32_f16_e32 v214, s39, v149
	v_perm_b32 v149, v148, v144, s31
	v_dot2c_f32_f16_e32 v211, s39, v117
	s_lshl_b32 s38, s38, 16
	v_and_b32_e32 v144, 0xf0f0f0f0, v150
	v_mov_b32_e32 v145, v146
	v_and_b32_e32 v146, 0xf0f0f0f0, v146
	s_or_b32 s37, s38, s37
	v_perm_b32 v148, v145, v150, s29
	v_dot2c_f32_f16_e32 v224, s37, v148
	v_perm_b32 v148, v146, v144, s29
	v_dot2c_f32_f16_e32 v220, s37, v148
	v_perm_b32 v148, v145, v150, s30
	v_dot2c_f32_f16_e32 v225, s37, v148
	v_perm_b32 v148, v146, v144, s30
	v_dot2c_f32_f16_e32 v221, s37, v148
	v_perm_b32 v148, v145, v150, s31
	v_perm_b32 v117, v145, v150, s33
	v_dot2c_f32_f16_e32 v223, s37, v117
	v_perm_b32 v117, v146, v144, s33
	v_dot2c_f32_f16_e32 v222, s37, v148
	v_perm_b32 v148, v146, v144, s31
	v_dot2c_f32_f16_e32 v219, s37, v117
	v_and_b32_e32 v144, 0xf0f0f0f0, v151
	v_mov_b32_e32 v145, v147
	v_and_b32_e32 v146, 0xf0f0f0f0, v147
	v_perm_b32 v147, v145, v151, s29
	v_dot2c_f32_f16_e32 v216, s37, v147
	v_perm_b32 v147, v146, v144, s29
	v_dot2c_f32_f16_e32 v212, s37, v147
	v_perm_b32 v147, v145, v151, s30
	v_dot2c_f32_f16_e32 v217, s37, v147
	v_perm_b32 v147, v146, v144, s30
	v_dot2c_f32_f16_e32 v213, s37, v147
	v_perm_b32 v147, v145, v151, s31
	v_perm_b32 v117, v145, v151, s33
	v_dot2c_f32_f16_e32 v215, s37, v117
	v_perm_b32 v117, v146, v144, s33
	v_dot2c_f32_f16_e32 v214, s37, v147
	v_perm_b32 v147, v146, v144, s31
	v_dot2c_f32_f16_e32 v211, s37, v117
	s_lshl_b32 s36, s36, 16
	v_mov_b32_e32 v117, v118
	v_and_b32_e32 v118, 0xf0f0f0f0, v118
	v_mov_b32_e32 v144, v114
	v_and_b32_e32 v114, 0xf0f0f0f0, v114
	s_or_b32 s35, s36, s35
	v_perm_b32 v145, v144, v117, s29
	v_dot2c_f32_f16_e32 v224, s35, v145
	v_perm_b32 v145, v114, v118, s29
	v_dot2c_f32_f16_e32 v220, s35, v145
	v_perm_b32 v145, v144, v117, s30
	v_dot2c_f32_f16_e32 v225, s35, v145
	v_perm_b32 v145, v114, v118, s30
	v_dot2c_f32_f16_e32 v221, s35, v145
	v_perm_b32 v145, v144, v117, s31
	v_dot2c_f32_f16_e32 v222, s35, v145
	v_perm_b32 v145, v114, v118, s31
	v_perm_b32 v117, v144, v117, s33
	v_perm_b32 v114, v114, v118, s33
	v_dot2c_f32_f16_e32 v223, s35, v117
	v_dot2c_f32_f16_e32 v219, s35, v114
	v_mov_b32_e32 v114, v119
	v_and_b32_e32 v117, 0xf0f0f0f0, v119
	v_mov_b32_e32 v118, v115
	v_and_b32_e32 v115, 0xf0f0f0f0, v115
	v_perm_b32 v119, v118, v114, s29
	v_dot2c_f32_f16_e32 v216, s35, v119
	v_perm_b32 v119, v115, v117, s29
	v_dot2c_f32_f16_e32 v212, s35, v119
	v_perm_b32 v119, v118, v114, s30
	v_dot2c_f32_f16_e32 v217, s35, v119
	v_perm_b32 v119, v115, v117, s30
	v_dot2c_f32_f16_e32 v213, s35, v119
	v_perm_b32 v119, v118, v114, s31
	v_perm_b32 v114, v118, v114, s33
	v_dot2c_f32_f16_e32 v215, s35, v114
	v_perm_b32 v114, v115, v117, s33
	v_dot2c_f32_f16_e32 v214, s35, v119
	v_perm_b32 v119, v115, v117, s31
	v_dot2c_f32_f16_e32 v211, s35, v114
	s_lshl_b32 s5, s5, 16
	v_mov_b32_e32 v114, v72
	v_and_b32_e32 v72, 0xf0f0f0f0, v72
	v_mov_b32_e32 v115, v68
	v_and_b32_e32 v68, 0xf0f0f0f0, v68
	s_or_b32 s4, s5, s4
	v_perm_b32 v117, v115, v114, s29
	v_dot2c_f32_f16_e32 v224, s4, v117
	v_perm_b32 v117, v68, v72, s29
	v_dot2c_f32_f16_e32 v220, s4, v117
	v_perm_b32 v117, v115, v114, s30
	v_dot2c_f32_f16_e32 v225, s4, v117
	v_perm_b32 v117, v68, v72, s30
	v_dot2c_f32_f16_e32 v221, s4, v117
	v_perm_b32 v117, v115, v114, s31
	v_dot2c_f32_f16_e32 v222, s4, v117
	v_perm_b32 v117, v68, v72, s31
	v_perm_b32 v68, v68, v72, s33
	v_perm_b32 v114, v115, v114, s33
	v_dot2c_f32_f16_e32 v219, s4, v68
	v_mov_b32_e32 v68, v73
	v_and_b32_e32 v72, 0xf0f0f0f0, v73
	v_mov_b32_e32 v73, v69
	v_and_b32_e32 v69, 0xf0f0f0f0, v69
	v_dot2c_f32_f16_e32 v223, s4, v114
	v_perm_b32 v114, v73, v68, s29
	v_dot2c_f32_f16_e32 v216, s4, v114
	v_perm_b32 v114, v69, v72, s29
	v_dot2c_f32_f16_e32 v212, s4, v114
	v_perm_b32 v114, v73, v68, s30
	v_dot2c_f32_f16_e32 v217, s4, v114
	v_perm_b32 v114, v69, v72, s30
	v_dot2c_f32_f16_e32 v213, s4, v114
	v_perm_b32 v114, v73, v68, s31
	v_perm_b32 v68, v73, v68, s33
	v_dot2c_f32_f16_e32 v215, s4, v68
	s_waitcnt vmcnt(31)
	v_dot8_i32_i4 v68, v248, v62, 0
	v_dot8_i32_i4 v68, v250, v63, v68
	v_dot2c_f32_f16_e32 v210, s39, v149
	v_dot2c_f32_f16_e32 v218, s37, v148
	v_dot2c_f32_f16_e32 v210, s37, v147
	v_lshlrev_b32_e32 v68, 4, v68
	v_dot8_i32_i4 v68, v247, v62, v68
	s_waitcnt vmcnt(30)
	v_dot8_i32_i4 v62, v248, v58, 0
	v_dot8_i32_i4 v62, v250, v59, v62
	v_dot8_i32_i4 v68, v249, v63, v68
	v_dot2c_f32_f16_e32 v218, s35, v145
	v_dot2c_f32_f16_e32 v210, s35, v119
	v_lshlrev_b32_e32 v62, 4, v62
	v_dot8_i32_i4 v62, v247, v58, v62
	s_waitcnt vmcnt(29)
	v_dot8_i32_i4 v58, v248, v54, 0
	v_dot8_i32_i4 v58, v250, v55, v58
	v_dot8_i32_i4 v62, v249, v59, v62
	v_dot2c_f32_f16_e32 v214, s4, v114
	v_perm_b32 v114, v69, v72, s31
	v_lshlrev_b32_e32 v58, 4, v58
	v_dot8_i32_i4 v58, v247, v54, v58
	s_waitcnt vmcnt(28)
	v_dot8_i32_i4 v54, v248, v50, 0
	v_dot8_i32_i4 v54, v250, v51, v54
	v_dot8_i32_i4 v58, v249, v55, v58
	v_dot2c_f32_f16_e32 v218, s4, v117
	v_dot2c_f32_f16_e32 v210, s4, v114
	v_lshlrev_b32_e32 v54, 4, v54
	v_dot8_i32_i4 v54, v247, v50, v54
	s_waitcnt vmcnt(27)
	v_dot8_i32_i4 v50, v248, v46, 0
	v_dot8_i32_i4 v50, v250, v47, v50
	v_dot8_i32_i4 v54, v249, v51, v54
	s_add_i32 s24, s25, 2
	s_cmp_lt_u32 s25, 5
	v_lshlrev_b32_e32 v50, 4, v50
	v_dot8_i32_i4 v50, v247, v46, v50
	s_waitcnt vmcnt(26)
	v_dot8_i32_i4 v46, v248, v42, 0
	v_dot8_i32_i4 v46, v250, v43, v46
	v_dot8_i32_i4 v50, v249, v47, v50
	v_cvt_f32_f16_e32 v116, v116
	s_nop 0
	v_lshlrev_b32_e32 v46, 4, v46
	v_dot8_i32_i4 v46, v247, v42, v46
	s_waitcnt vmcnt(25)
	v_dot8_i32_i4 v42, v248, v38, 0
	v_dot8_i32_i4 v42, v250, v39, v42
	v_dot8_i32_i4 v46, v249, v43, v46
	s_nop 1
	v_lshlrev_b32_e32 v42, 4, v42
	v_dot8_i32_i4 v42, v247, v38, v42
	s_waitcnt vmcnt(24)
	v_dot8_i32_i4 v38, v248, v30, 0
	v_dot8_i32_i4 v38, v250, v31, v38
	v_dot8_i32_i4 v42, v249, v39, v42
	s_nop 1
	v_lshlrev_b32_e32 v38, 4, v38
	v_dot8_i32_i4 v38, v247, v30, v38
	v_dot8_i32_i4 v38, v249, v31, v38
	s_waitcnt vmcnt(22)
	v_dot8_i32_i4 v31, v248, v22, 0
	v_dot8_i32_i4 v31, v250, v23, v31
	v_dot8_i32_i4 v30, v248, v34, 0
	v_dot8_i32_i4 v30, v250, v35, v30
	s_nop 0
	v_lshlrev_b32_e32 v31, 4, v31
	v_dot8_i32_i4 v31, v247, v22, v31
	v_dot8_i32_i4 v31, v249, v23, v31
	s_waitcnt vmcnt(20)
	v_dot8_i32_i4 v23, v248, v14, 0
	v_dot8_i32_i4 v23, v250, v15, v23
	v_dot8_i32_i4 v22, v248, v26, 0
	v_dot8_i32_i4 v22, v250, v27, v22
	s_nop 0
	v_lshlrev_b32_e32 v23, 4, v23
	v_dot8_i32_i4 v23, v247, v14, v23
	v_dot8_i32_i4 v23, v249, v15, v23
	s_waitcnt vmcnt(18)
	v_dot8_i32_i4 v15, v248, v6, 0
	v_dot8_i32_i4 v15, v250, v7, v15
	v_dot8_i32_i4 v14, v248, v18, 0
	v_dot8_i32_i4 v14, v250, v19, v14
	s_nop 0
	v_lshlrev_b32_e32 v15, 4, v15
	v_dot8_i32_i4 v15, v247, v6, v15
	v_dot8_i32_i4 v15, v249, v7, v15
	s_waitcnt vmcnt(17)
	v_dot8_i32_i4 v6, v248, v10, 0
	s_waitcnt vmcnt(16)
	v_dot8_i32_i4 v7, v248, v2, 0
	v_dot8_i32_i4 v6, v250, v11, v6
	v_dot8_i32_i4 v7, v250, v3, v7
	v_lshlrev_b32_e32 v30, 4, v30
	v_lshlrev_b32_e32 v22, 4, v22
	v_lshlrev_b32_e32 v14, 4, v14
	v_lshlrev_b32_e32 v6, 4, v6
	v_lshlrev_b32_e32 v7, 4, v7
	v_dot8_i32_i4 v30, v247, v34, v30
	v_dot8_i32_i4 v22, v247, v26, v22
	v_dot8_i32_i4 v14, v247, v18, v14
	v_dot8_i32_i4 v6, v247, v10, v6
	v_dot8_i32_i4 v7, v247, v2, v7
	v_dot8_i32_i4 v30, v249, v35, v30
	v_dot8_i32_i4 v22, v249, v27, v22
	v_dot8_i32_i4 v14, v249, v19, v14
	v_dot8_i32_i4 v6, v249, v11, v6
	v_dot8_i32_i4 v7, v249, v3, v7
	v_permlane32_swap_b32_e32 v68, v30
	v_permlane32_swap_b32_e32 v62, v31
	v_permlane32_swap_b32_e32 v58, v22
	v_permlane32_swap_b32_e32 v54, v23
	v_permlane32_swap_b32_e32 v50, v14
	v_permlane32_swap_b32_e32 v46, v15
	v_permlane32_swap_b32_e32 v42, v6
	v_permlane32_swap_b32_e32 v38, v7
	v_add_u32_e32 v2, v68, v30
	v_add_u32_e32 v3, v62, v31
	v_add_u32_e32 v10, v58, v22
	v_add_u32_e32 v11, v54, v23
	v_add_u32_e32 v14, v50, v14
	v_add_u32_e32 v15, v46, v15
	v_add_u32_e32 v6, v42, v6
	v_add_u32_e32 v7, v38, v7
	v_permlane16_swap_b32_e32 v2, v14
	v_permlane16_swap_b32_e32 v3, v15
	v_permlane16_swap_b32_e32 v10, v6
	v_permlane16_swap_b32_e32 v11, v7
	v_add_u32_e32 v2, v2, v14
	v_add_u32_e32 v3, v3, v15
	v_add_u32_e32 v6, v10, v6
	v_add_u32_e32 v7, v11, v7
	v_cndmask_b32_e64 v10, v6, v2, s[0:1]
	v_cndmask_b32_e64 v2, v2, v6, s[0:1]
	v_cndmask_b32_e64 v6, v7, v3, s[0:1]
	v_cndmask_b32_e64 v3, v3, v7, s[0:1]
	v_add_u32_dpp v2, v2, v10 quad_perm:[2,3,0,1] row_mask:0xf bank_mask:0xf bound_ctrl:1
	ds_bpermute_b32 v7, v66, v71 offset:64
	v_add_u32_dpp v3, v3, v6 quad_perm:[2,3,0,1] row_mask:0xf bank_mask:0xf bound_ctrl:1
	v_cndmask_b32_e64 v6, v3, v2, s[2:3]
	v_cndmask_b32_e64 v2, v2, v3, s[2:3]
	ds_bpermute_b32 v3, v66, v70 offset:64
	v_add_f32_e32 v68, v252, v116
	v_add_u32_dpp v2, v2, v6 quad_perm:[1,0,3,2] row_mask:0xf bank_mask:0xf bound_ctrl:1
	v_perm_b32 v6, v69, v72, s33
	v_dot2c_f32_f16_e32 v211, s4, v6
	v_add_u32_dpp v2, v2, v2 row_ror:8 row_mask:0xf bank_mask:0xf bound_ctrl:1
	ds_bpermute_b32 v6, v66, v67 offset:64
	s_nop 0
	v_add_u32_dpp v2, v2, v2 row_ror:4 row_mask:0xf bank_mask:0xf bound_ctrl:1
	v_cvt_f32_i32_e32 v2, v2
	v_add_f32_e32 v2, v251, v2
	v_mul_f32_e32 v2, v244, v2
	s_waitcnt lgkmcnt(1)
	v_mul_f32_e32 v2, v2, v3
	v_fma_f32 v3, |v2|, s28, 1.0
	v_rcp_f32_e32 v3, v3
	v_mul_f32_e32 v11, v2, v2
	v_mul_f32_e32 v11, 0xbf38aa3b, v11
	v_exp_f32_e32 v11, v11
	v_fmamk_f32 v10, v3, 0x3f07dc22, v227
	v_fmaak_f32 v10, v3, v10, 0x3f35f0e3
	v_fmaak_f32 v10, v3, v10, 0xbe11a98e
	v_fmaak_f32 v10, v3, v10, 0x3e027906
	v_mul_f32_e32 v3, v3, v10
	v_mul_f32_e32 v3, v11, v3
	v_mul_f32_e32 v10, v2, v3
	v_fma_f32 v3, -v2, v3, v2
	v_cmp_gt_f32_e64 s[4:5], 0, v2
	v_and_b32_e32 v11, 0xf0f0f0f0, v60
	s_nop 0
	v_cndmask_b32_e64 v2, v3, v10, s[4:5]
	s_waitcnt lgkmcnt(0)
	v_mul_f32_e32 v2, v2, v6
	v_mul_f32_e32 v2, v2, v7
	v_fma_mixlo_f16 v2, v2, s16, 0
	v_and_b32_e32 v3, 0xffff, v2
	s_cselect_b64 s[4:5], -1, 0
	v_readlane_b32 s25, v3, 1
	v_cvt_f32_f16_e32 v66, v2
	v_cndmask_b32_e64 v2, v242, v232, s[4:5]
	v_readlane_b32 s5, v3, 0
	s_lshl_b32 s25, s25, 16
	v_and_b32_e32 v7, 0xf0f0f0f0, v64
	s_or_b32 s5, s25, s5
	v_perm_b32 v14, v60, v64, s29
	v_dot2c_f32_f16_e32 v224, s5, v14
	v_perm_b32 v14, v11, v7, s29
	v_dot2c_f32_f16_e32 v220, s5, v14
	v_perm_b32 v14, v60, v64, s30
	v_dot2c_f32_f16_e32 v225, s5, v14
	v_perm_b32 v14, v11, v7, s30
	v_dot2c_f32_f16_e32 v221, s5, v14
	v_perm_b32 v14, v60, v64, s31
	v_perm_b32 v6, v60, v64, s33
	v_dot2c_f32_f16_e32 v223, s5, v6
	v_perm_b32 v6, v11, v7, s33
	v_dot2c_f32_f16_e32 v222, s5, v14
	v_perm_b32 v14, v11, v7, s31
	v_dot2c_f32_f16_e32 v219, s5, v6
	v_and_b32_e32 v7, 0xf0f0f0f0, v65
	v_and_b32_e32 v11, 0xf0f0f0f0, v61
	v_dot2c_f32_f16_e32 v218, s5, v14
	v_perm_b32 v14, v61, v65, s29
	v_dot2c_f32_f16_e32 v216, s5, v14
	v_perm_b32 v14, v11, v7, s29
	v_dot2c_f32_f16_e32 v212, s5, v14
	v_perm_b32 v14, v61, v65, s30
	v_dot2c_f32_f16_e32 v217, s5, v14
	v_perm_b32 v14, v11, v7, s30
	v_dot2c_f32_f16_e32 v213, s5, v14
	v_perm_b32 v14, v61, v65, s31
	v_perm_b32 v6, v61, v65, s33
	v_dot2c_f32_f16_e32 v214, s5, v14
	v_perm_b32 v14, v11, v7, s31
	v_dot2c_f32_f16_e32 v215, s5, v6
	v_perm_b32 v6, v11, v7, s33
	v_cndmask_b32_e32 v2, v2, v231, vcc
	v_dot2c_f32_f16_e32 v210, s5, v14
	v_dot2c_f32_f16_e32 v211, s5, v6
	s_add_i32 s4, s21, 16
	v_readlane_b32 s4, v2, s4
	s_nop 1
	v_lshl_or_b32 v6, s4, 10, v194
	s_add_i32 s4, s21, 17
	v_readlane_b32 s4, v2, s4
	s_nop 1
	v_lshl_or_b32 v7, s4, 10, v194
	global_load_dwordx4 v[62:65], v6, s[10:11]
	global_load_dwordx4 v[58:61], v7, s[10:11]
	v_readlane_b32 s5, v3, 3
	v_readlane_b32 s4, v3, 2
	s_lshl_b32 s5, s5, 16
	v_and_b32_e32 v7, 0xf0f0f0f0, v56
	v_and_b32_e32 v11, 0xf0f0f0f0, v52
	s_or_b32 s4, s5, s4
	v_perm_b32 v14, v52, v56, s29
	v_dot2c_f32_f16_e32 v224, s4, v14
	v_perm_b32 v14, v11, v7, s29
	v_dot2c_f32_f16_e32 v220, s4, v14
	v_perm_b32 v14, v52, v56, s30
	v_dot2c_f32_f16_e32 v225, s4, v14
	v_perm_b32 v14, v11, v7, s30
	v_dot2c_f32_f16_e32 v221, s4, v14
	v_perm_b32 v14, v52, v56, s31
	v_perm_b32 v6, v52, v56, s33
	v_dot2c_f32_f16_e32 v223, s4, v6
	v_perm_b32 v6, v11, v7, s33
	v_dot2c_f32_f16_e32 v222, s4, v14
	v_perm_b32 v14, v11, v7, s31
	v_dot2c_f32_f16_e32 v219, s4, v6
	v_and_b32_e32 v7, 0xf0f0f0f0, v57
	v_and_b32_e32 v11, 0xf0f0f0f0, v53
	v_dot2c_f32_f16_e32 v218, s4, v14
	v_perm_b32 v14, v53, v57, s29
	v_dot2c_f32_f16_e32 v216, s4, v14
	v_perm_b32 v14, v11, v7, s29
	v_dot2c_f32_f16_e32 v212, s4, v14
	v_perm_b32 v14, v53, v57, s30
	v_dot2c_f32_f16_e32 v217, s4, v14
	v_perm_b32 v14, v11, v7, s30
	v_dot2c_f32_f16_e32 v213, s4, v14
	v_perm_b32 v14, v53, v57, s31
	v_perm_b32 v6, v53, v57, s33
	v_dot2c_f32_f16_e32 v214, s4, v14
	v_perm_b32 v14, v11, v7, s31
	v_dot2c_f32_f16_e32 v215, s4, v6
	v_perm_b32 v6, v11, v7, s33
	v_dot2c_f32_f16_e32 v210, s4, v14
	v_dot2c_f32_f16_e32 v211, s4, v6
	s_add_i32 s4, s21, 18
	v_readlane_b32 s4, v2, s4
	s_nop 1
	v_lshl_or_b32 v6, s4, 10, v194
	s_add_i32 s4, s21, 19
	v_readlane_b32 s4, v2, s4
	s_nop 1
	v_lshl_or_b32 v7, s4, 10, v194
	global_load_dwordx4 v[54:57], v6, s[10:11]
	global_load_dwordx4 v[50:53], v7, s[10:11]
	v_readlane_b32 s5, v3, 17
	v_readlane_b32 s4, v3, 16
	s_lshl_b32 s5, s5, 16
	v_and_b32_e32 v7, 0xf0f0f0f0, v48
	v_and_b32_e32 v11, 0xf0f0f0f0, v44
	s_or_b32 s4, s5, s4
	v_perm_b32 v14, v44, v48, s29
	v_dot2c_f32_f16_e32 v224, s4, v14
	v_perm_b32 v14, v11, v7, s29
	v_dot2c_f32_f16_e32 v220, s4, v14
	v_perm_b32 v14, v44, v48, s30
	v_dot2c_f32_f16_e32 v225, s4, v14
	v_perm_b32 v14, v11, v7, s30
	v_dot2c_f32_f16_e32 v221, s4, v14
	v_perm_b32 v14, v44, v48, s31
	v_perm_b32 v6, v44, v48, s33
	v_dot2c_f32_f16_e32 v223, s4, v6
	v_perm_b32 v6, v11, v7, s33
	v_dot2c_f32_f16_e32 v222, s4, v14
	v_perm_b32 v14, v11, v7, s31
	v_dot2c_f32_f16_e32 v219, s4, v6
	v_and_b32_e32 v7, 0xf0f0f0f0, v49
	v_and_b32_e32 v11, 0xf0f0f0f0, v45
	v_dot2c_f32_f16_e32 v218, s4, v14
	v_perm_b32 v14, v45, v49, s29
	v_dot2c_f32_f16_e32 v216, s4, v14
	v_perm_b32 v14, v11, v7, s29
	v_dot2c_f32_f16_e32 v212, s4, v14
	v_perm_b32 v14, v45, v49, s30
	v_dot2c_f32_f16_e32 v217, s4, v14
	v_perm_b32 v14, v11, v7, s30
	v_dot2c_f32_f16_e32 v213, s4, v14
	v_perm_b32 v14, v45, v49, s31
	v_perm_b32 v6, v45, v49, s33
	v_dot2c_f32_f16_e32 v214, s4, v14
	v_perm_b32 v14, v11, v7, s31
	v_dot2c_f32_f16_e32 v215, s4, v6
	v_perm_b32 v6, v11, v7, s33
	v_dot2c_f32_f16_e32 v210, s4, v14
	v_dot2c_f32_f16_e32 v211, s4, v6
	s_add_i32 s4, s21, 20
	v_readlane_b32 s4, v2, s4
	s_nop 1
	v_lshl_or_b32 v6, s4, 10, v194
	s_add_i32 s4, s21, 21
	v_readlane_b32 s4, v2, s4
	s_nop 1
	v_lshl_or_b32 v7, s4, 10, v194
	global_load_dwordx4 v[46:49], v6, s[10:11]
	global_load_dwordx4 v[42:45], v7, s[10:11]
	v_readlane_b32 s5, v3, 19
	v_readlane_b32 s4, v3, 18
	s_lshl_b32 s5, s5, 16
	v_and_b32_e32 v7, 0xf0f0f0f0, v40
	v_and_b32_e32 v11, 0xf0f0f0f0, v32
	s_or_b32 s4, s5, s4
	v_perm_b32 v14, v32, v40, s29
	v_dot2c_f32_f16_e32 v224, s4, v14
	v_perm_b32 v14, v11, v7, s29
	v_dot2c_f32_f16_e32 v220, s4, v14
	v_perm_b32 v14, v32, v40, s30
	v_dot2c_f32_f16_e32 v225, s4, v14
	v_perm_b32 v14, v11, v7, s30
	v_dot2c_f32_f16_e32 v221, s4, v14
	v_perm_b32 v14, v32, v40, s31
	v_perm_b32 v6, v32, v40, s33
	v_dot2c_f32_f16_e32 v223, s4, v6
	v_perm_b32 v6, v11, v7, s33
	v_dot2c_f32_f16_e32 v222, s4, v14
	v_perm_b32 v14, v11, v7, s31
	v_dot2c_f32_f16_e32 v219, s4, v6
	v_and_b32_e32 v7, 0xf0f0f0f0, v41
	v_and_b32_e32 v11, 0xf0f0f0f0, v33
	v_dot2c_f32_f16_e32 v218, s4, v14
	v_perm_b32 v14, v33, v41, s29
	v_dot2c_f32_f16_e32 v216, s4, v14
	v_perm_b32 v14, v11, v7, s29
	v_dot2c_f32_f16_e32 v212, s4, v14
	v_perm_b32 v14, v33, v41, s30
	v_dot2c_f32_f16_e32 v217, s4, v14
	v_perm_b32 v14, v11, v7, s30
	v_dot2c_f32_f16_e32 v213, s4, v14
	v_perm_b32 v14, v33, v41, s31
	v_perm_b32 v6, v33, v41, s33
	v_dot2c_f32_f16_e32 v214, s4, v14
	v_perm_b32 v14, v11, v7, s31
	v_dot2c_f32_f16_e32 v215, s4, v6
	v_perm_b32 v6, v11, v7, s33
	v_dot2c_f32_f16_e32 v210, s4, v14
	v_dot2c_f32_f16_e32 v211, s4, v6
	s_add_i32 s4, s21, 22
	v_readlane_b32 s4, v2, s4
	s_nop 1
	v_lshl_or_b32 v6, s4, 10, v194
	s_add_i32 s4, s21, 23
	v_readlane_b32 s4, v2, s4
	s_nop 1
	v_lshl_or_b32 v7, s4, 10, v194
	global_load_dwordx4 v[38:41], v6, s[10:11]
	global_load_dwordx4 v[30:33], v7, s[10:11]
	v_readlane_b32 s5, v3, 33
	v_readlane_b32 s4, v3, 32
	s_lshl_b32 s5, s5, 16
	v_and_b32_e32 v7, 0xf0f0f0f0, v36
	v_and_b32_e32 v11, 0xf0f0f0f0, v24
	s_or_b32 s4, s5, s4
	v_perm_b32 v14, v24, v36, s29
	v_dot2c_f32_f16_e32 v224, s4, v14
	v_perm_b32 v14, v11, v7, s29
	v_dot2c_f32_f16_e32 v220, s4, v14
	v_perm_b32 v14, v24, v36, s30
	v_dot2c_f32_f16_e32 v225, s4, v14
	v_perm_b32 v14, v11, v7, s30
	v_dot2c_f32_f16_e32 v221, s4, v14
	v_perm_b32 v14, v24, v36, s31
	v_perm_b32 v6, v24, v36, s33
	v_dot2c_f32_f16_e32 v223, s4, v6
	v_perm_b32 v6, v11, v7, s33
	v_dot2c_f32_f16_e32 v222, s4, v14
	v_perm_b32 v14, v11, v7, s31
	v_dot2c_f32_f16_e32 v219, s4, v6
	v_and_b32_e32 v7, 0xf0f0f0f0, v37
	v_and_b32_e32 v11, 0xf0f0f0f0, v25
	v_dot2c_f32_f16_e32 v218, s4, v14
	v_perm_b32 v14, v25, v37, s29
	v_dot2c_f32_f16_e32 v216, s4, v14
	v_perm_b32 v14, v11, v7, s29
	v_dot2c_f32_f16_e32 v212, s4, v14
	v_perm_b32 v14, v25, v37, s30
	v_dot2c_f32_f16_e32 v217, s4, v14
	v_perm_b32 v14, v11, v7, s30
	v_dot2c_f32_f16_e32 v213, s4, v14
	v_perm_b32 v14, v25, v37, s31
	v_perm_b32 v6, v25, v37, s33
	v_dot2c_f32_f16_e32 v214, s4, v14
	v_perm_b32 v14, v11, v7, s31
	v_dot2c_f32_f16_e32 v215, s4, v6
	v_perm_b32 v6, v11, v7, s33
	v_dot2c_f32_f16_e32 v210, s4, v14
	v_dot2c_f32_f16_e32 v211, s4, v6
	s_add_i32 s4, s21, 24
	v_readlane_b32 s4, v2, s4
	s_nop 1
	v_lshl_or_b32 v6, s4, 10, v194
	s_add_i32 s4, s21, 25
	v_readlane_b32 s4, v2, s4
	s_nop 1
	v_lshl_or_b32 v7, s4, 10, v194
	global_load_dwordx4 v[34:37], v6, s[10:11]
	global_load_dwordx4 v[22:25], v7, s[10:11]
	v_readlane_b32 s5, v3, 35
	v_readlane_b32 s4, v3, 34
	s_lshl_b32 s5, s5, 16
	v_and_b32_e32 v7, 0xf0f0f0f0, v28
	v_and_b32_e32 v11, 0xf0f0f0f0, v16
	s_or_b32 s4, s5, s4
	v_perm_b32 v14, v16, v28, s29
	v_dot2c_f32_f16_e32 v224, s4, v14
	v_perm_b32 v14, v11, v7, s29
	v_dot2c_f32_f16_e32 v220, s4, v14
	v_perm_b32 v14, v16, v28, s30
	v_dot2c_f32_f16_e32 v225, s4, v14
	v_perm_b32 v14, v11, v7, s30
	v_dot2c_f32_f16_e32 v221, s4, v14
	v_perm_b32 v14, v16, v28, s31
	v_perm_b32 v6, v16, v28, s33
	v_dot2c_f32_f16_e32 v223, s4, v6
	v_perm_b32 v6, v11, v7, s33
	v_dot2c_f32_f16_e32 v222, s4, v14
	v_perm_b32 v14, v11, v7, s31
	v_dot2c_f32_f16_e32 v219, s4, v6
	v_and_b32_e32 v7, 0xf0f0f0f0, v29
	v_and_b32_e32 v11, 0xf0f0f0f0, v17
	v_dot2c_f32_f16_e32 v218, s4, v14
	v_perm_b32 v14, v17, v29, s29
	v_dot2c_f32_f16_e32 v216, s4, v14
	v_perm_b32 v14, v11, v7, s29
	v_dot2c_f32_f16_e32 v212, s4, v14
	v_perm_b32 v14, v17, v29, s30
	v_dot2c_f32_f16_e32 v217, s4, v14
	v_perm_b32 v14, v11, v7, s30
	v_dot2c_f32_f16_e32 v213, s4, v14
	v_perm_b32 v14, v17, v29, s31
	v_perm_b32 v6, v17, v29, s33
	v_dot2c_f32_f16_e32 v214, s4, v14
	v_perm_b32 v14, v11, v7, s31
	v_dot2c_f32_f16_e32 v215, s4, v6
	v_perm_b32 v6, v11, v7, s33
	v_dot2c_f32_f16_e32 v210, s4, v14
	v_dot2c_f32_f16_e32 v211, s4, v6
	s_add_i32 s4, s21, 26
	v_readlane_b32 s4, v2, s4
	s_nop 1
	v_lshl_or_b32 v6, s4, 10, v194
	s_add_i32 s4, s21, 27
	v_readlane_b32 s4, v2, s4
	s_nop 1
	v_lshl_or_b32 v7, s4, 10, v194
	global_load_dwordx4 v[26:29], v6, s[10:11]
	global_load_dwordx4 v[14:17], v7, s[10:11]
	v_readlane_b32 s5, v3, 49
	v_readlane_b32 s4, v3, 48
	s_lshl_b32 s5, s5, 16
	v_and_b32_e32 v7, 0xf0f0f0f0, v20
	v_mov_b32_e32 v10, v8
	v_and_b32_e32 v8, 0xf0f0f0f0, v8
	s_or_b32 s4, s5, s4
	v_perm_b32 v11, v10, v20, s29
	v_dot2c_f32_f16_e32 v224, s4, v11
	v_perm_b32 v11, v8, v7, s29
	v_dot2c_f32_f16_e32 v220, s4, v11
	v_perm_b32 v11, v10, v20, s30
	v_dot2c_f32_f16_e32 v225, s4, v11
	v_perm_b32 v11, v8, v7, s30
	v_dot2c_f32_f16_e32 v221, s4, v11
	v_perm_b32 v11, v10, v20, s31
	v_perm_b32 v6, v10, v20, s33
	v_dot2c_f32_f16_e32 v223, s4, v6
	v_perm_b32 v6, v8, v7, s33
	v_dot2c_f32_f16_e32 v222, s4, v11
	v_perm_b32 v11, v8, v7, s31
	v_dot2c_f32_f16_e32 v219, s4, v6
	v_and_b32_e32 v7, 0xf0f0f0f0, v21
	v_mov_b32_e32 v8, v9
	v_and_b32_e32 v9, 0xf0f0f0f0, v9
	v_perm_b32 v10, v8, v21, s29
	v_dot2c_f32_f16_e32 v216, s4, v10
	v_perm_b32 v10, v9, v7, s29
	v_dot2c_f32_f16_e32 v212, s4, v10
	v_perm_b32 v10, v8, v21, s30
	v_dot2c_f32_f16_e32 v217, s4, v10
	v_perm_b32 v10, v9, v7, s30
	v_dot2c_f32_f16_e32 v213, s4, v10
	v_perm_b32 v10, v8, v21, s31
	v_perm_b32 v6, v8, v21, s33
	v_dot2c_f32_f16_e32 v214, s4, v10
	v_perm_b32 v10, v9, v7, s31
	v_dot2c_f32_f16_e32 v215, s4, v6
	v_perm_b32 v6, v9, v7, s33
	v_dot2c_f32_f16_e32 v218, s4, v11
	v_dot2c_f32_f16_e32 v210, s4, v10
	v_dot2c_f32_f16_e32 v211, s4, v6
	s_add_i32 s4, s21, 28
	v_readlane_b32 s4, v2, s4
	s_nop 1
	v_lshl_or_b32 v6, s4, 10, v194
	s_add_i32 s4, s21, 29
	v_readlane_b32 s4, v2, s4
	s_nop 1
	v_lshl_or_b32 v7, s4, 10, v194
	global_load_dwordx4 v[18:21], v6, s[10:11]
	s_nop 0
	global_load_dwordx4 v[6:9], v7, s[10:11]
	v_readlane_b32 s5, v3, 51
	v_readlane_b32 s4, v3, 50
	s_lshl_b32 s5, s5, 16
	v_mov_b32_e32 v3, v12
	v_and_b32_e32 v10, 0xf0f0f0f0, v12
	v_mov_b32_e32 v11, v4
	v_and_b32_e32 v4, 0xf0f0f0f0, v4
	s_or_b32 s4, s5, s4
	v_perm_b32 v12, v11, v3, s29
	v_dot2c_f32_f16_e32 v224, s4, v12
	v_perm_b32 v12, v4, v10, s29
	v_dot2c_f32_f16_e32 v220, s4, v12
	v_perm_b32 v12, v11, v3, s30
	v_dot2c_f32_f16_e32 v225, s4, v12
	v_perm_b32 v12, v4, v10, s30
	v_dot2c_f32_f16_e32 v221, s4, v12
	v_perm_b32 v12, v11, v3, s31
	v_perm_b32 v3, v11, v3, s33
	v_dot2c_f32_f16_e32 v223, s4, v3
	v_perm_b32 v3, v4, v10, s33
	v_dot2c_f32_f16_e32 v222, s4, v12
	v_perm_b32 v12, v4, v10, s31
	v_dot2c_f32_f16_e32 v219, s4, v3
	v_and_b32_e32 v4, 0xf0f0f0f0, v13
	v_mov_b32_e32 v10, v5
	v_and_b32_e32 v5, 0xf0f0f0f0, v5
	v_perm_b32 v11, v10, v13, s29
	v_dot2c_f32_f16_e32 v216, s4, v11
	v_perm_b32 v11, v5, v4, s29
	v_dot2c_f32_f16_e32 v212, s4, v11
	v_perm_b32 v11, v10, v13, s30
	v_dot2c_f32_f16_e32 v217, s4, v11
	v_perm_b32 v11, v5, v4, s30
	v_dot2c_f32_f16_e32 v213, s4, v11
	v_perm_b32 v11, v10, v13, s31
	v_perm_b32 v3, v10, v13, s33
	v_dot2c_f32_f16_e32 v214, s4, v11
	v_perm_b32 v11, v5, v4, s31
	v_dot2c_f32_f16_e32 v215, s4, v3
	v_perm_b32 v3, v5, v4, s33
	v_dot2c_f32_f16_e32 v218, s4, v12
	v_dot2c_f32_f16_e32 v210, s4, v11
	v_dot2c_f32_f16_e32 v211, s4, v3
	s_add_i32 s4, s21, 30
	v_readlane_b32 s4, v2, s4
	s_nop 1
	v_lshl_or_b32 v3, s4, 10, v194
	s_add_i32 s4, s21, 31
	v_readlane_b32 s4, v2, s4
	s_nop 1
	v_lshl_or_b32 v2, s4, 10, v194
	global_load_dwordx4 v[10:13], v3, s[10:11]
	s_nop 0
	global_load_dwordx4 v[2:5], v2, s[10:11]
	v_add_f32_e32 v252, v68, v66
	s_add_i32 s21, s21, 32
	s_and_b64 vcc, exec, s[22:23]
	s_cbranch_vccnz .LBB0_1013
	s_waitcnt vmcnt(23)
	v_mov_b64_e32 v[158:159], v[112:113]
	v_mov_b64_e32 v[190:191], v[80:81]
	v_mov_b64_e32 v[186:187], v[76:77]
	v_mov_b64_e32 v[182:183], v[88:89]
	v_mov_b64_e32 v[178:179], v[84:85]
	v_mov_b64_e32 v[174:175], v[96:97]
	v_mov_b64_e32 v[170:171], v[92:93]
	v_mov_b64_e32 v[166:167], v[104:105]
	v_mov_b64_e32 v[162:163], v[100:101]
	v_mov_b64_e32 v[156:157], v[110:111]
	s_waitcnt vmcnt(22)
	v_mov_b64_e32 v[154:155], v[108:109]
	s_waitcnt vmcnt(21)
	v_mov_b64_e32 v[150:151], v[126:127]
	s_waitcnt vmcnt(20)
	v_mov_b64_e32 v[146:147], v[122:123]
	s_waitcnt vmcnt(19)
	v_mov_b64_e32 v[116:117], v[132:133]
	s_waitcnt vmcnt(18)
	v_mov_b64_e32 v[112:113], v[128:129]
	s_waitcnt vmcnt(17)
	v_mov_b64_e32 v[70:71], v[140:141]
	s_waitcnt vmcnt(16)
	v_mov_b64_e32 v[66:67], v[136:137]
	v_mov_b64_e32 v[188:189], v[78:79]
	v_mov_b64_e32 v[184:185], v[74:75]
	v_mov_b64_e32 v[180:181], v[86:87]
	v_mov_b64_e32 v[176:177], v[82:83]
	v_mov_b64_e32 v[172:173], v[94:95]
	v_mov_b64_e32 v[168:169], v[90:91]
	v_mov_b64_e32 v[164:165], v[102:103]
	v_mov_b64_e32 v[160:161], v[98:99]
	v_mov_b64_e32 v[152:153], v[106:107]
	v_mov_b64_e32 v[148:149], v[124:125]
	v_mov_b64_e32 v[144:145], v[120:121]
	v_mov_b64_e32 v[118:119], v[134:135]
	v_mov_b64_e32 v[114:115], v[130:131]
	v_mov_b64_e32 v[72:73], v[142:143]
	v_mov_b64_e32 v[68:69], v[138:139]
	s_mov_b32 s25, s24
	s_branch .LBB0_1019
